# serialized load-wait-store epilogue chains de-serialized (attention, ssd_out, merge GEMM mid+final, wout GEMM): gain loads issued ahead into free registers with counted vmcnt; plus scans and lists cha
# speedup vs baseline: 1.0177x; 1.0110x over previous
.LBB0_281:
	v_readlane_b32 s42, v253, 26
	v_readlane_b32 s43, v253, 27
	s_andn2_b64 vcc, exec, s[42:43]
	v_readlane_b32 s70, v254, 49
	v_mov_b32_e32 v228, v226
	v_mov_b64_e32 v[236:237], 0x200
	v_mov_b64_e32 v[248:249], 0x1ff
	s_waitcnt vmcnt(7)
	v_mov_b32_e32 v178, v212
	s_waitcnt lgkmcnt(0)
	s_barrier
	s_cbranch_vccnz .LBB0_260
	v_readlane_b32 s12, v253, 30
	s_mul_i32 s18, s20, 0xc00
	s_add_u32 s10, s10, s18
	v_lshl_add_u32 v156, v240, 2, s12
	ds_read2st64_b32 v[2:3], v156 offset1:1
	ds_read2st64_b32 v[4:5], v156 offset0:2 offset1:3
	ds_read2st64_b32 v[6:7], v156 offset0:4 offset1:5
	ds_read2st64_b32 v[8:9], v156 offset0:6 offset1:7
	s_mul_hi_u32 s12, s20, 0xc00
	s_waitcnt lgkmcnt(3)
	v_fma_f32 v148, v129, v0, -v3
	v_fma_f32 v153, v128, v0, -v2
	v_mul_f32_e32 v157, v148, v148
	v_fmac_f32_e32 v157, v153, v153
	s_waitcnt lgkmcnt(2)
	v_fma_f32 v154, v130, v0, -v4
	v_fmac_f32_e32 v157, v154, v154
	v_fma_f32 v155, v131, v0, -v5
	ds_read2st64_b32 v[2:3], v156 offset0:8 offset1:9
	v_fmac_f32_e32 v157, v155, v155
	s_waitcnt lgkmcnt(2)
	v_fma_f32 v144, v132, v0, -v6
	v_fmac_f32_e32 v157, v144, v144
	v_fma_f32 v145, v133, v0, -v7
	v_fmac_f32_e32 v157, v145, v145
	s_waitcnt lgkmcnt(1)
	v_fma_f32 v146, v134, v0, -v8
	v_fmac_f32_e32 v157, v146, v146
	v_fma_f32 v147, v135, v0, -v9
	ds_read2st64_b32 v[4:5], v156 offset0:10 offset1:11
	ds_read2st64_b32 v[6:7], v156 offset0:12 offset1:13
	ds_read2st64_b32 v[8:9], v156 offset0:14 offset1:15
	v_fmac_f32_e32 v157, v147, v147
	s_waitcnt lgkmcnt(3)
	v_fma_f32 v149, v136, v0, -v2
	v_fmac_f32_e32 v157, v149, v149
	v_fma_f32 v150, v137, v0, -v3
	v_fmac_f32_e32 v157, v150, v150
	s_waitcnt lgkmcnt(2)
	v_fma_f32 v151, v138, v0, -v4
	v_fmac_f32_e32 v157, v151, v151
	v_fma_f32 v152, v139, v0, -v5
	ds_read2st64_b32 v[2:3], v156 offset0:16 offset1:17
	v_fmac_f32_e32 v157, v152, v152
	s_waitcnt lgkmcnt(2)
	v_fma_f32 v136, v140, v0, -v6
	v_fmac_f32_e32 v157, v136, v136
	v_fma_f32 v137, v141, v0, -v7
	v_fmac_f32_e32 v157, v137, v137
	s_waitcnt lgkmcnt(1)
	v_fma_f32 v138, v142, v0, -v8
	v_fmac_f32_e32 v157, v138, v138
	v_fma_f32 v139, v143, v0, -v9
	ds_read2st64_b32 v[4:5], v156 offset0:18 offset1:19
	ds_read2st64_b32 v[6:7], v156 offset0:20 offset1:21
	ds_read2st64_b32 v[8:9], v156 offset0:22 offset1:23
	v_fmac_f32_e32 v157, v139, v139
	s_waitcnt lgkmcnt(3)
	v_fma_f32 v140, v112, v0, -v2
	v_fmac_f32_e32 v157, v140, v140
	v_fma_f32 v141, v113, v0, -v3
	v_fmac_f32_e32 v157, v141, v141
	s_waitcnt lgkmcnt(2)
	v_fma_f32 v142, v114, v0, -v4
	ds_read2st64_b32 v[2:3], v156 offset0:24 offset1:25
	v_fmac_f32_e32 v157, v142, v142
	v_fma_f32 v143, v115, v0, -v5
	v_fmac_f32_e32 v157, v143, v143
	s_waitcnt lgkmcnt(2)
	v_fma_f32 v128, v116, v0, -v6
	v_fmac_f32_e32 v157, v128, v128
	v_fma_f32 v129, v117, v0, -v7
	v_fmac_f32_e32 v157, v129, v129
	s_waitcnt lgkmcnt(1)
	v_fma_f32 v130, v118, v0, -v8
	v_fmac_f32_e32 v157, v130, v130
	v_fma_f32 v131, v119, v0, -v9
	ds_read2st64_b32 v[4:5], v156 offset0:26 offset1:27
	ds_read2st64_b32 v[6:7], v156 offset0:28 offset1:29
	ds_read2st64_b32 v[8:9], v156 offset0:30 offset1:31
	s_waitcnt lgkmcnt(3)
	v_fma_f32 v132, v120, v0, -v2
	v_fma_f32 v133, v121, v0, -v3
	ds_read2st64_b32 v[2:3], v156 offset0:32 offset1:33
	v_fmac_f32_e32 v157, v131, v131
	v_fmac_f32_e32 v157, v132, v132
	v_fmac_f32_e32 v157, v133, v133
	s_waitcnt lgkmcnt(3)
	v_fma_f32 v134, v122, v0, -v4
	v_fmac_f32_e32 v157, v134, v134
	v_fma_f32 v135, v123, v0, -v5
	v_fmac_f32_e32 v157, v135, v135
	s_waitcnt lgkmcnt(2)
	v_fma_f32 v120, v124, v0, -v6
	v_fma_f32 v121, v125, v0, -v7
	s_waitcnt lgkmcnt(1)
	v_fma_f32 v122, v126, v0, -v8
	v_fma_f32 v123, v127, v0, -v9
	ds_read2st64_b32 v[4:5], v156 offset0:34 offset1:35
	ds_read2st64_b32 v[6:7], v156 offset0:36 offset1:37
	ds_read2st64_b32 v[8:9], v156 offset0:38 offset1:39
	s_waitcnt lgkmcnt(3)
	v_fma_f32 v124, v96, v0, -v2
	v_fma_f32 v125, v97, v0, -v3
	ds_read2st64_b32 v[2:3], v156 offset0:40 offset1:41
	v_fmac_f32_e32 v157, v120, v120
	v_fmac_f32_e32 v157, v121, v121
	v_fmac_f32_e32 v157, v122, v122
	v_fmac_f32_e32 v157, v123, v123
	v_fmac_f32_e32 v157, v124, v124
	s_waitcnt lgkmcnt(3)
	v_fma_f32 v126, v98, v0, -v4
	v_fma_f32 v127, v99, v0, -v5
	s_waitcnt lgkmcnt(2)
	v_fma_f32 v112, v100, v0, -v6
	v_fma_f32 v113, v101, v0, -v7
	s_waitcnt lgkmcnt(1)
	v_fma_f32 v114, v102, v0, -v8
	v_fma_f32 v115, v103, v0, -v9
	ds_read2st64_b32 v[4:5], v156 offset0:42 offset1:43
	ds_read2st64_b32 v[6:7], v156 offset0:44 offset1:45
	ds_read2st64_b32 v[8:9], v156 offset0:46 offset1:47
	s_waitcnt lgkmcnt(3)
	v_fma_f32 v116, v104, v0, -v2
	v_fma_f32 v117, v105, v0, -v3
	ds_read2st64_b32 v[2:3], v156 offset0:48 offset1:49
	v_fmac_f32_e32 v157, v125, v125
	v_fmac_f32_e32 v157, v126, v126
	v_fmac_f32_e32 v157, v127, v127
	v_fmac_f32_e32 v157, v112, v112
	v_fmac_f32_e32 v157, v113, v113
	s_waitcnt lgkmcnt(3)
	v_fma_f32 v118, v106, v0, -v4
	v_fma_f32 v119, v107, v0, -v5
	s_waitcnt lgkmcnt(2)
	v_fma_f32 v104, v108, v0, -v6
	v_fma_f32 v105, v109, v0, -v7
	s_waitcnt lgkmcnt(1)
	v_fma_f32 v106, v110, v0, -v8
	v_fma_f32 v107, v111, v0, -v9
	ds_read2st64_b32 v[4:5], v156 offset0:50 offset1:51
	ds_read2st64_b32 v[6:7], v156 offset0:52 offset1:53
	ds_read2st64_b32 v[8:9], v156 offset0:54 offset1:55
	s_waitcnt lgkmcnt(3)
	v_fma_f32 v108, v80, v0, -v2
	v_fma_f32 v109, v81, v0, -v3
	ds_read2st64_b32 v[2:3], v156 offset0:56 offset1:57
	v_fmac_f32_e32 v157, v114, v114
	v_fmac_f32_e32 v157, v115, v115
	v_fmac_f32_e32 v157, v116, v116
	v_fmac_f32_e32 v157, v117, v117
	v_fmac_f32_e32 v157, v118, v118
	s_waitcnt lgkmcnt(3)
	v_fma_f32 v110, v82, v0, -v4
	v_fma_f32 v111, v83, v0, -v5
	s_waitcnt lgkmcnt(2)
	v_fma_f32 v96, v84, v0, -v6
	v_fma_f32 v97, v85, v0, -v7
	s_waitcnt lgkmcnt(1)
	v_fma_f32 v98, v86, v0, -v8
	v_fma_f32 v99, v87, v0, -v9
	ds_read2st64_b32 v[4:5], v156 offset0:58 offset1:59
	ds_read2st64_b32 v[6:7], v156 offset0:60 offset1:61
	ds_read2st64_b32 v[8:9], v156 offset0:62 offset1:63
	s_waitcnt lgkmcnt(3)
	v_fma_f32 v100, v88, v0, -v2
	v_fma_f32 v101, v89, v0, -v3
	ds_read2st64_b32 v[2:3], v156 offset0:64 offset1:65
	v_fmac_f32_e32 v157, v119, v119
	v_fmac_f32_e32 v157, v104, v104
	v_fmac_f32_e32 v157, v105, v105
	v_fmac_f32_e32 v157, v106, v106
	v_fmac_f32_e32 v157, v107, v107
	s_waitcnt lgkmcnt(3)
	v_fma_f32 v102, v90, v0, -v4
	v_fma_f32 v103, v91, v0, -v5
	s_waitcnt lgkmcnt(2)
	v_fma_f32 v86, v92, v0, -v6
	v_fma_f32 v87, v93, v0, -v7
	s_waitcnt lgkmcnt(1)
	v_fma_f32 v88, v94, v0, -v8
	v_fma_f32 v89, v95, v0, -v9
	ds_read2st64_b32 v[4:5], v156 offset0:66 offset1:67
	ds_read2st64_b32 v[6:7], v156 offset0:68 offset1:69
	ds_read2st64_b32 v[8:9], v156 offset0:70 offset1:71
	s_waitcnt lgkmcnt(3)
	v_fma_f32 v90, v64, v0, -v2
	v_fma_f32 v91, v65, v0, -v3
	ds_read2st64_b32 v[2:3], v156 offset0:72 offset1:73
	v_fmac_f32_e32 v157, v108, v108
	v_fmac_f32_e32 v157, v109, v109
	v_fmac_f32_e32 v157, v110, v110
	v_fmac_f32_e32 v157, v111, v111
	v_fmac_f32_e32 v157, v96, v96
	s_waitcnt lgkmcnt(3)
	v_fma_f32 v92, v66, v0, -v4
	v_fma_f32 v93, v67, v0, -v5
	s_waitcnt lgkmcnt(2)
	v_fma_f32 v80, v68, v0, -v6
	v_fma_f32 v81, v69, v0, -v7
	s_waitcnt lgkmcnt(1)
	v_fma_f32 v82, v70, v0, -v8
	v_fma_f32 v83, v71, v0, -v9
	ds_read2st64_b32 v[4:5], v156 offset0:74 offset1:75
	ds_read2st64_b32 v[6:7], v156 offset0:76 offset1:77
	ds_read2st64_b32 v[8:9], v156 offset0:78 offset1:79
	s_waitcnt lgkmcnt(3)
	v_fma_f32 v84, v72, v0, -v2
	v_fma_f32 v85, v73, v0, -v3
	ds_read2st64_b32 v[2:3], v156 offset0:80 offset1:81
	v_fmac_f32_e32 v157, v97, v97
	v_fmac_f32_e32 v157, v98, v98
	v_fmac_f32_e32 v157, v99, v99
	v_fmac_f32_e32 v157, v100, v100
	v_fmac_f32_e32 v157, v101, v101
	s_waitcnt lgkmcnt(3)
	v_fma_f32 v74, v74, v0, -v4
	v_fma_f32 v75, v75, v0, -v5
	s_waitcnt lgkmcnt(2)
	v_fma_f32 v66, v76, v0, -v6
	v_fma_f32 v67, v77, v0, -v7
	s_waitcnt lgkmcnt(1)
	v_fma_f32 v68, v78, v0, -v8
	v_fma_f32 v69, v79, v0, -v9
	ds_read2st64_b32 v[4:5], v156 offset0:82 offset1:83
	ds_read2st64_b32 v[6:7], v156 offset0:84 offset1:85
	ds_read2st64_b32 v[8:9], v156 offset0:86 offset1:87
	s_waitcnt lgkmcnt(3)
	v_fma_f32 v70, v48, v0, -v2
	v_fma_f32 v71, v49, v0, -v3
	ds_read2st64_b32 v[2:3], v156 offset0:88 offset1:89
	v_fmac_f32_e32 v157, v102, v102
	v_fmac_f32_e32 v157, v103, v103
	v_fmac_f32_e32 v157, v86, v86
	v_fmac_f32_e32 v157, v87, v87
	v_fmac_f32_e32 v157, v88, v88
	s_waitcnt lgkmcnt(3)
	v_fma_f32 v72, v50, v0, -v4
	v_fma_f32 v73, v51, v0, -v5
	s_waitcnt lgkmcnt(2)
	v_fma_f32 v64, v52, v0, -v6
	v_fma_f32 v65, v53, v0, -v7
	s_waitcnt lgkmcnt(1)
	v_fma_f32 v54, v54, v0, -v8
	v_fma_f32 v55, v55, v0, -v9
	ds_read2st64_b32 v[4:5], v156 offset0:90 offset1:91
	ds_read2st64_b32 v[6:7], v156 offset0:92 offset1:93
	ds_read2st64_b32 v[8:9], v156 offset0:94 offset1:95
	s_waitcnt lgkmcnt(3)
	v_fma_f32 v56, v56, v0, -v2
	v_fma_f32 v57, v57, v0, -v3
	ds_read2st64_b32 v[2:3], v156 offset0:96 offset1:97
	v_fmac_f32_e32 v157, v89, v89
	v_fmac_f32_e32 v157, v90, v90
	v_fmac_f32_e32 v157, v91, v91
	v_fmac_f32_e32 v157, v92, v92
	v_fmac_f32_e32 v157, v93, v93
	s_waitcnt lgkmcnt(3)
	v_fma_f32 v58, v58, v0, -v4
	v_fma_f32 v59, v59, v0, -v5
	s_waitcnt lgkmcnt(2)
	v_fma_f32 v48, v60, v0, -v6
	v_fma_f32 v49, v61, v0, -v7
	s_waitcnt lgkmcnt(1)
	v_fma_f32 v50, v62, v0, -v8
	v_fma_f32 v51, v63, v0, -v9
	ds_read2st64_b32 v[4:5], v156 offset0:98 offset1:99
	ds_read2st64_b32 v[6:7], v156 offset0:100 offset1:101
	ds_read2st64_b32 v[8:9], v156 offset0:102 offset1:103
	s_waitcnt lgkmcnt(3)
	v_fma_f32 v52, v32, v0, -v2
	v_fma_f32 v53, v33, v0, -v3
	ds_read2st64_b32 v[2:3], v156 offset0:104 offset1:105
	v_fmac_f32_e32 v157, v80, v80
	v_fmac_f32_e32 v157, v81, v81
	v_fmac_f32_e32 v157, v82, v82
	v_fmac_f32_e32 v157, v83, v83
	v_fmac_f32_e32 v157, v84, v84
	s_waitcnt lgkmcnt(3)
	v_fma_f32 v34, v34, v0, -v4
	v_fma_f32 v35, v35, v0, -v5
	s_waitcnt lgkmcnt(2)
	v_fma_f32 v10, v36, v0, -v6
	v_fma_f32 v11, v37, v0, -v7
	s_waitcnt lgkmcnt(1)
	v_fma_f32 v12, v38, v0, -v8
	v_fma_f32 v13, v39, v0, -v9
	ds_read2st64_b32 v[4:5], v156 offset0:106 offset1:107
	ds_read2st64_b32 v[6:7], v156 offset0:108 offset1:109
	ds_read2st64_b32 v[8:9], v156 offset0:110 offset1:111
	s_waitcnt lgkmcnt(3)
	v_fma_f32 v14, v40, v0, -v2
	v_fma_f32 v15, v41, v0, -v3
	ds_read2st64_b32 v[2:3], v156 offset0:112 offset1:113
	v_fmac_f32_e32 v157, v85, v85
	v_fmac_f32_e32 v157, v74, v74
	v_fmac_f32_e32 v157, v75, v75
	v_fmac_f32_e32 v157, v66, v66
	v_fmac_f32_e32 v157, v67, v67
	s_waitcnt lgkmcnt(3)
	v_fma_f32 v32, v42, v0, -v4
	s_waitcnt lgkmcnt(2)
	v_fma_f32 v4, v44, v0, -v6
	s_waitcnt lgkmcnt(1)
	v_fma_f32 v6, v46, v0, -v8
	s_waitcnt lgkmcnt(0)
	v_fma_f32 v8, v16, v0, -v2
	v_ashrrev_i32_e32 v2, 3, v240
	v_fmac_f32_e32 v157, v68, v68
	v_and_b32_e32 v62, -4, v2
	v_fmac_f32_e32 v157, v69, v69
	v_ashrrev_i32_e32 v63, 31, v62
	v_fmac_f32_e32 v157, v70, v70
	v_fma_f32 v33, v43, v0, -v5
	v_fma_f32 v5, v45, v0, -v7
	v_fma_f32 v7, v47, v0, -v9
	v_fma_f32 v9, v17, v0, -v3
	v_lshl_add_u64 v[2:3], v[62:63], 2, s[40:41]
	v_fmac_f32_e32 v157, v71, v71
	ds_read2st64_b32 v[36:37], v156 offset0:114 offset1:115
	ds_read2st64_b32 v[46:47], v156 offset0:116 offset1:117
	ds_read2st64_b32 v[60:61], v156 offset0:118 offset1:119
	global_load_dwordx4 v[42:45], v[2:3], off
	global_load_dwordx4 v[160:163], v[2:3], off offset:32
	global_load_dwordx4 v[164:167], v[2:3], off offset:64
	global_load_dwordx4 v[168:171], v[2:3], off offset:96
	global_load_dwordx4 v[172:175], v[2:3], off offset:128
	global_load_dwordx4 v[180:183], v[2:3], off offset:160
	global_load_dwordx4 v[184:187], v[2:3], off offset:192
	global_load_dwordx4 v[188:191], v[2:3], off offset:224
	global_load_dwordx4 v[192:195], v[2:3], off offset:256
	global_load_dwordx4 v[196:199], v[2:3], off offset:288
	global_load_dwordx4 v[200:203], v[2:3], off offset:320
	global_load_dwordx4 v[204:207], v[2:3], off offset:352
	v_fmac_f32_e32 v157, v72, v72
	v_fmac_f32_e32 v157, v73, v73
	v_fmac_f32_e32 v157, v64, v64
	v_fmac_f32_e32 v157, v65, v65
	v_fmac_f32_e32 v157, v54, v54
	v_fmac_f32_e32 v157, v55, v55
	v_fmac_f32_e32 v157, v56, v56
	v_fmac_f32_e32 v157, v57, v57
	v_fmac_f32_e32 v157, v58, v58
	v_fmac_f32_e32 v157, v59, v59
	v_fmac_f32_e32 v157, v48, v48
	v_fmac_f32_e32 v157, v49, v49
	v_fmac_f32_e32 v157, v50, v50
	v_fmac_f32_e32 v157, v51, v51
	v_fmac_f32_e32 v157, v52, v52
	v_fmac_f32_e32 v157, v53, v53
	v_fmac_f32_e32 v157, v34, v34
	v_fmac_f32_e32 v157, v35, v35
	v_fmac_f32_e32 v157, v10, v10
	v_fmac_f32_e32 v157, v11, v11
	v_fmac_f32_e32 v157, v12, v12
	v_fmac_f32_e32 v157, v13, v13
	v_fmac_f32_e32 v157, v14, v14
	v_fmac_f32_e32 v157, v15, v15
	v_fmac_f32_e32 v157, v32, v32
	v_fmac_f32_e32 v157, v33, v33
	v_fmac_f32_e32 v157, v4, v4
	v_fmac_f32_e32 v157, v5, v5
	v_fmac_f32_e32 v157, v6, v6
	v_fmac_f32_e32 v157, v7, v7
	v_fmac_f32_e32 v157, v8, v8
	v_fmac_f32_e32 v157, v9, v9
	s_waitcnt lgkmcnt(2)
	v_fma_f32 v39, v18, v0, -v36
	v_fmac_f32_e32 v157, v39, v39
	v_fma_f32 v40, v19, v0, -v37
	ds_read2st64_b32 v[16:17], v156 offset0:120 offset1:121
	v_fmac_f32_e32 v157, v40, v40
	s_waitcnt lgkmcnt(2)
	v_fma_f32 v36, v20, v0, -v46
	v_fmac_f32_e32 v157, v36, v36
	v_fma_f32 v37, v21, v0, -v47
	v_fmac_f32_e32 v157, v37, v37
	s_waitcnt lgkmcnt(1)
	v_fma_f32 v38, v22, v0, -v60
	v_fmac_f32_e32 v157, v38, v38
	v_fma_f32 v23, v23, v0, -v61
	ds_read2st64_b32 v[46:47], v156 offset0:122 offset1:123
	ds_read2st64_b32 v[60:61], v156 offset0:124 offset1:125
	ds_read2st64_b32 v[76:77], v156 offset0:126 offset1:127
	v_fmac_f32_e32 v157, v23, v23
	s_waitcnt lgkmcnt(3)
	v_fma_f32 v19, v24, v0, -v16
	v_fmac_f32_e32 v157, v19, v19
	v_fma_f32 v20, v25, v0, -v17
	v_fmac_f32_e32 v157, v20, v20
	s_waitcnt lgkmcnt(2)
	v_fma_f32 v21, v26, v0, -v46
	v_fmac_f32_e32 v157, v21, v21
	v_fma_f32 v22, v27, v0, -v47
	v_fmac_f32_e32 v157, v22, v22
	s_waitcnt lgkmcnt(1)
	v_fma_f32 v16, v28, v0, -v60
	v_fmac_f32_e32 v157, v16, v16
	v_fma_f32 v17, v29, v0, -v61
	v_fmac_f32_e32 v157, v17, v17
	s_waitcnt lgkmcnt(0)
	v_fma_f32 v18, v30, v0, -v76
	v_fmac_f32_e32 v157, v18, v18
	v_fma_f32 v0, v31, v0, -v77
	v_fmac_f32_e32 v157, v0, v0
	v_mov_b32_e32 v24, v157
	s_nop 1
	v_permlane32_swap_b32_e32 v157, v24
	v_add_f32_e32 v24, v157, v24
	v_fmamk_f32 v24, v24, 0x3b800000, v210
	v_mul_f32_e32 v25, 0x4f800000, v24
	v_cmp_gt_f32_e32 vcc, s25, v24
	s_addc_u32 s11, s11, s12
	s_add_u32 s10, s10, s30
	v_cndmask_b32_e32 v24, v24, v25, vcc
	v_sqrt_f32_e32 v25, v24
	s_movk_i32 s4, 0xc00
	s_addc_u32 s11, s11, 0
	v_mov_b32_e32 v31, v1
	v_add_u32_e32 v26, -1, v25
	v_fma_f32 v27, -v26, v25, v24
	v_cmp_ge_f32_e64 s[40:41], 0, v27
	v_add_u32_e32 v27, 1, v25
	s_nop 0
	v_cndmask_b32_e64 v26, v25, v26, s[40:41]
	v_fma_f32 v25, -v27, v25, v24
	v_cmp_lt_f32_e64 s[40:41], 0, v25
	s_nop 1
	v_cndmask_b32_e64 v25, v26, v27, s[40:41]
	v_mul_f32_e32 v26, 0x37800000, v25
	v_cndmask_b32_e32 v25, v25, v26, vcc
	v_cmp_class_f32_e32 vcc, v24, v211
	s_nop 1
	v_cndmask_b32_e32 v24, v25, v24, vcc
	v_div_scale_f32 v25, s[40:41], v24, v24, v227
	v_rcp_f32_e32 v26, v25
	s_nop 0
	v_fma_f32 v27, -v25, v26, 1.0
	v_fmac_f32_e32 v26, v27, v26
	v_div_scale_f32 v27, vcc, v227, v24, v227
	v_mul_f32_e32 v28, v27, v26
	v_fma_f32 v29, -v25, v28, v27
	v_fmac_f32_e32 v28, v29, v26
	v_fma_f32 v25, -v25, v28, v27
	v_div_fmas_f32 v25, v25, v26, v28
	v_div_fixup_f32 v24, v25, v24, v227
	v_mul_f32_e32 v25, v153, v24
	v_mul_f32_e32 v26, v148, v24
	s_waitcnt vmcnt(11)
	v_mul_f32_e32 v25, v42, v25
	v_mul_f32_e32 v26, v43, v26
	v_med3_f32 v25, v25, s19, v229
	v_med3_f32 v26, v26, s19, v229
	v_mov_b32_e32 v29, v1
	v_cvt_pk_fp8_f32 v29, v25, v26
	v_mul_f32_e32 v27, v154, v24
	v_mul_f32_e32 v28, v155, v24
	v_mul_f32_e32 v27, v44, v27
	v_mul_f32_e32 v25, v45, v28
	v_med3_f32 v26, v27, s19, v229
	v_med3_f32 v25, v25, s19, v229
	v_cvt_pk_fp8_f32 v29, v26, v25 op_sel:[0,0,1]
	v_and_b32_e32 v25, 31, v240
	v_mad_u32_u24 v25, v25, s4, v62
	v_mul_f32_e32 v30, v144, v24
	global_store_dword v25, v29, s[10:11]
	v_mul_f32_e32 v41, v137, v24
	v_mul_f32_e32 v42, v138, v24
	v_mul_f32_e32 v43, v139, v24
	v_mul_f32_e32 v34, v34, v24
	v_mul_f32_e32 v35, v35, v24
	v_mul_f32_e32 v10, v10, v24
	v_mul_f32_e32 v11, v11, v24
	v_mul_f32_e32 v12, v12, v24
	v_mul_f32_e32 v13, v13, v24
	v_mul_f32_e32 v14, v14, v24
	v_mul_f32_e32 v15, v15, v24
	v_mul_f32_e32 v4, v4, v24
	v_mul_f32_e32 v5, v5, v24
	v_mul_f32_e32 v6, v6, v24
	v_mul_f32_e32 v7, v7, v24
	v_mul_f32_e32 v8, v8, v24
	v_mul_f32_e32 v9, v9, v24
	v_mul_f32_e32 v0, v0, v24
	s_waitcnt vmcnt(11)
	v_mul_f32_e32 v26, v160, v30
	v_mul_f32_e32 v30, v145, v24
	v_mul_f32_e32 v27, v161, v30
	v_med3_f32 v26, v26, s19, v229
	v_med3_f32 v27, v27, s19, v229
	v_mul_f32_e32 v30, v146, v24
	v_cvt_pk_fp8_f32 v31, v26, v27
	v_mul_f32_e32 v28, v162, v30
	v_mul_f32_e32 v30, v147, v24
	v_mul_f32_e32 v26, v163, v30
	v_med3_f32 v27, v28, s19, v229
	v_med3_f32 v26, v26, s19, v229
	v_cvt_pk_fp8_f32 v31, v27, v26 op_sel:[0,0,1]
	v_mul_f32_e32 v30, v149, v24
	global_store_dword v25, v31, s[10:11] offset:8
	global_load_dwordx4 v[160:163], v[2:3], off offset:384
	v_mov_b32_e32 v31, v1
	s_waitcnt vmcnt(12)
	v_mul_f32_e32 v26, v30, v164
	v_mul_f32_e32 v30, v150, v24
	v_mul_f32_e32 v27, v30, v165
	v_med3_f32 v26, v26, s19, v229
	v_med3_f32 v27, v27, s19, v229
	v_mul_f32_e32 v30, v151, v24
	v_cvt_pk_fp8_f32 v31, v26, v27
	v_mul_f32_e32 v28, v30, v166
	v_mul_f32_e32 v30, v152, v24
	v_mul_f32_e32 v26, v30, v167
	v_med3_f32 v27, v28, s19, v229
	v_med3_f32 v26, v26, s19, v229
	v_cvt_pk_fp8_f32 v31, v27, v26 op_sel:[0,0,1]
	v_mov_b32_e32 v30, v1
	global_store_dword v25, v31, s[10:11] offset:16
	global_load_dwordx4 v[164:167], v[2:3], off offset:416
	v_mul_f32_e32 v31, v136, v24
	s_waitcnt vmcnt(13)
	v_mul_f32_e32 v26, v31, v168
	v_mul_f32_e32 v27, v41, v169
	v_med3_f32 v26, v26, s19, v229
	v_med3_f32 v27, v27, s19, v229
	v_cvt_pk_fp8_f32 v30, v26, v27
	v_mul_f32_e32 v28, v42, v170
	v_mul_f32_e32 v26, v43, v171
	v_med3_f32 v27, v28, s19, v229
	v_med3_f32 v26, v26, s19, v229
	v_cvt_pk_fp8_f32 v30, v27, v26 op_sel:[0,0,1]
	v_mul_f32_e32 v31, v140, v24
	v_mul_f32_e32 v41, v141, v24
	v_mul_f32_e32 v42, v142, v24
	global_store_dword v25, v30, s[10:11] offset:24
	global_load_dwordx4 v[168:171], v[2:3], off offset:448
	v_mov_b32_e32 v30, v1
	v_mul_f32_e32 v43, v143, v24
	s_waitcnt vmcnt(14)
	v_mul_f32_e32 v26, v31, v172
	v_mul_f32_e32 v27, v41, v173
	v_med3_f32 v26, v26, s19, v229
	v_med3_f32 v27, v27, s19, v229
	v_cvt_pk_fp8_f32 v30, v26, v27
	v_mul_f32_e32 v28, v42, v174
	v_mul_f32_e32 v26, v43, v175
	v_med3_f32 v27, v28, s19, v229
	v_med3_f32 v26, v26, s19, v229
	v_cvt_pk_fp8_f32 v30, v27, v26 op_sel:[0,0,1]
	v_mul_f32_e32 v31, v128, v24
	v_mul_f32_e32 v41, v129, v24
	v_mul_f32_e32 v42, v130, v24
	global_store_dword v25, v30, s[10:11] offset:32
	global_load_dwordx4 v[172:175], v[2:3], off offset:480
	v_mov_b32_e32 v30, v1
	v_mul_f32_e32 v43, v131, v24
	s_waitcnt vmcnt(15)
	v_mul_f32_e32 v26, v31, v180
	v_mul_f32_e32 v27, v41, v181
	v_med3_f32 v26, v26, s19, v229
	v_med3_f32 v27, v27, s19, v229
	v_cvt_pk_fp8_f32 v30, v26, v27
	v_mul_f32_e32 v28, v42, v182
	v_mul_f32_e32 v26, v43, v183
	v_med3_f32 v27, v28, s19, v229
	v_med3_f32 v26, v26, s19, v229
	v_cvt_pk_fp8_f32 v30, v27, v26 op_sel:[0,0,1]
	v_mul_f32_e32 v31, v132, v24
	v_mul_f32_e32 v41, v133, v24
	v_mul_f32_e32 v42, v134, v24
	global_store_dword v25, v30, s[10:11] offset:40
	global_load_dwordx4 v[180:183], v[2:3], off offset:512
	v_mov_b32_e32 v30, v1
	v_mul_f32_e32 v43, v135, v24
	s_waitcnt vmcnt(16)
	v_mul_f32_e32 v26, v31, v184
	v_mul_f32_e32 v27, v41, v185
	v_med3_f32 v26, v26, s19, v229
	v_med3_f32 v27, v27, s19, v229
	v_cvt_pk_fp8_f32 v30, v26, v27
	v_mul_f32_e32 v28, v42, v186
	v_mul_f32_e32 v26, v43, v187
	v_med3_f32 v27, v28, s19, v229
	v_med3_f32 v26, v26, s19, v229
	v_cvt_pk_fp8_f32 v30, v27, v26 op_sel:[0,0,1]
	v_mul_f32_e32 v31, v120, v24
	v_mul_f32_e32 v41, v121, v24
	v_mul_f32_e32 v42, v122, v24
	global_store_dword v25, v30, s[10:11] offset:48
	global_load_dwordx4 v[184:187], v[2:3], off offset:544
	v_mov_b32_e32 v30, v1
	v_mul_f32_e32 v43, v123, v24
	s_waitcnt vmcnt(17)
	v_mul_f32_e32 v26, v31, v188
	v_mul_f32_e32 v27, v41, v189
	v_med3_f32 v26, v26, s19, v229
	v_med3_f32 v27, v27, s19, v229
	v_cvt_pk_fp8_f32 v30, v26, v27
	v_mul_f32_e32 v28, v42, v190
	v_mul_f32_e32 v26, v43, v191
	v_med3_f32 v27, v28, s19, v229
	v_med3_f32 v26, v26, s19, v229
	v_cvt_pk_fp8_f32 v30, v27, v26 op_sel:[0,0,1]
	v_mul_f32_e32 v31, v124, v24
	v_mul_f32_e32 v41, v125, v24
	v_mul_f32_e32 v42, v126, v24
	global_store_dword v25, v30, s[10:11] offset:56
	global_load_dwordx4 v[188:191], v[2:3], off offset:576
	v_mov_b32_e32 v30, v1
	v_mul_f32_e32 v43, v127, v24
	s_waitcnt vmcnt(18)
	v_mul_f32_e32 v26, v31, v192
	v_mul_f32_e32 v27, v41, v193
	v_med3_f32 v26, v26, s19, v229
	v_med3_f32 v27, v27, s19, v229
	v_cvt_pk_fp8_f32 v30, v26, v27
	v_mul_f32_e32 v28, v42, v194
	v_mul_f32_e32 v26, v43, v195
	v_med3_f32 v27, v28, s19, v229
	v_med3_f32 v26, v26, s19, v229
	v_cvt_pk_fp8_f32 v30, v27, v26 op_sel:[0,0,1]
	v_mul_f32_e32 v31, v112, v24
	v_mul_f32_e32 v41, v113, v24
	v_mul_f32_e32 v42, v114, v24
	global_store_dword v25, v30, s[10:11] offset:64
	global_load_dwordx4 v[192:195], v[2:3], off offset:608
	v_mov_b32_e32 v30, v1
	v_mul_f32_e32 v43, v115, v24
	s_waitcnt vmcnt(19)
	v_mul_f32_e32 v26, v31, v196
	v_mul_f32_e32 v27, v41, v197
	v_med3_f32 v26, v26, s19, v229
	v_med3_f32 v27, v27, s19, v229
	v_cvt_pk_fp8_f32 v30, v26, v27
	v_mul_f32_e32 v28, v42, v198
	v_mul_f32_e32 v26, v43, v199
	v_med3_f32 v27, v28, s19, v229
	v_med3_f32 v26, v26, s19, v229
	v_cvt_pk_fp8_f32 v30, v27, v26 op_sel:[0,0,1]
	v_mul_f32_e32 v31, v116, v24
	v_mul_f32_e32 v41, v117, v24
	v_mul_f32_e32 v42, v118, v24
	global_store_dword v25, v30, s[10:11] offset:72
	global_load_dwordx4 v[196:199], v[2:3], off offset:640
	v_mov_b32_e32 v30, v1
	v_mul_f32_e32 v43, v119, v24
	s_waitcnt vmcnt(20)
	v_mul_f32_e32 v26, v31, v200
	v_mul_f32_e32 v27, v41, v201
	v_med3_f32 v26, v26, s19, v229
	v_med3_f32 v27, v27, s19, v229
	v_cvt_pk_fp8_f32 v30, v26, v27
	v_mul_f32_e32 v28, v42, v202
	v_mul_f32_e32 v26, v43, v203
	v_med3_f32 v27, v28, s19, v229
	v_med3_f32 v26, v26, s19, v229
	v_cvt_pk_fp8_f32 v30, v27, v26 op_sel:[0,0,1]
	v_mul_f32_e32 v31, v104, v24
	v_mul_f32_e32 v41, v105, v24
	v_mul_f32_e32 v42, v106, v24
	global_store_dword v25, v30, s[10:11] offset:80
	global_load_dwordx4 v[200:203], v[2:3], off offset:672
	v_mov_b32_e32 v30, v1
	v_mul_f32_e32 v43, v107, v24
	s_waitcnt vmcnt(21)
	v_mul_f32_e32 v26, v31, v204
	v_mul_f32_e32 v27, v41, v205
	v_med3_f32 v26, v26, s19, v229
	v_med3_f32 v27, v27, s19, v229
	v_cvt_pk_fp8_f32 v30, v26, v27
	v_mul_f32_e32 v28, v42, v206
	v_mul_f32_e32 v26, v43, v207
	v_med3_f32 v27, v28, s19, v229
	v_med3_f32 v26, v26, s19, v229
	v_cvt_pk_fp8_f32 v30, v27, v26 op_sel:[0,0,1]
	v_mul_f32_e32 v31, v108, v24
	v_mul_f32_e32 v41, v109, v24
	v_mul_f32_e32 v42, v110, v24
	global_store_dword v25, v30, s[10:11] offset:88
	global_load_dwordx4 v[204:207], v[2:3], off offset:704
	v_mov_b32_e32 v30, v1
	v_mul_f32_e32 v43, v111, v24
	s_waitcnt vmcnt(20)
	v_mul_f32_e32 v26, v31, v160
	v_mul_f32_e32 v27, v41, v161
	v_med3_f32 v26, v26, s19, v229
	v_med3_f32 v27, v27, s19, v229
	v_cvt_pk_fp8_f32 v30, v26, v27
	v_mul_f32_e32 v28, v42, v162
	v_mul_f32_e32 v26, v43, v163
	v_med3_f32 v27, v28, s19, v229
	v_med3_f32 v26, v26, s19, v229
	v_cvt_pk_fp8_f32 v30, v27, v26 op_sel:[0,0,1]
	v_mul_f32_e32 v31, v96, v24
	v_mul_f32_e32 v41, v97, v24
	v_mul_f32_e32 v42, v98, v24
	global_store_dword v25, v30, s[10:11] offset:96
	global_load_dwordx4 v[160:163], v[2:3], off offset:736
	v_mov_b32_e32 v30, v1
	v_mul_f32_e32 v43, v99, v24
	s_waitcnt vmcnt(20)
	v_mul_f32_e32 v26, v31, v164
	v_mul_f32_e32 v27, v41, v165
	v_med3_f32 v26, v26, s19, v229
	v_med3_f32 v27, v27, s19, v229
	v_cvt_pk_fp8_f32 v30, v26, v27
	v_mul_f32_e32 v28, v42, v166
	v_mul_f32_e32 v26, v43, v167
	v_med3_f32 v27, v28, s19, v229
	v_med3_f32 v26, v26, s19, v229
	v_cvt_pk_fp8_f32 v30, v27, v26 op_sel:[0,0,1]
	v_mul_f32_e32 v31, v100, v24
	v_mul_f32_e32 v41, v101, v24
	v_mul_f32_e32 v42, v102, v24
	global_store_dword v25, v30, s[10:11] offset:104
	global_load_dwordx4 v[164:167], v[2:3], off offset:768
	v_mov_b32_e32 v30, v1
	v_mul_f32_e32 v43, v103, v24
	s_waitcnt vmcnt(20)
	v_mul_f32_e32 v26, v31, v168
	v_mul_f32_e32 v27, v41, v169
	v_med3_f32 v26, v26, s19, v229
	v_med3_f32 v27, v27, s19, v229
	v_cvt_pk_fp8_f32 v30, v26, v27
	v_mul_f32_e32 v28, v42, v170
	v_mul_f32_e32 v26, v43, v171
	v_med3_f32 v27, v28, s19, v229
	v_med3_f32 v26, v26, s19, v229
	v_cvt_pk_fp8_f32 v30, v27, v26 op_sel:[0,0,1]
	v_mul_f32_e32 v31, v86, v24
	v_mul_f32_e32 v41, v87, v24
	v_mul_f32_e32 v42, v88, v24
	global_store_dword v25, v30, s[10:11] offset:112
	global_load_dwordx4 v[168:171], v[2:3], off offset:800
	v_mov_b32_e32 v30, v1
	v_mul_f32_e32 v43, v89, v24
	s_waitcnt vmcnt(20)
	v_mul_f32_e32 v26, v31, v172
	v_mul_f32_e32 v27, v41, v173
	v_med3_f32 v26, v26, s19, v229
	v_med3_f32 v27, v27, s19, v229
	v_cvt_pk_fp8_f32 v30, v26, v27
	v_mul_f32_e32 v28, v42, v174
	v_mul_f32_e32 v26, v43, v175
	v_med3_f32 v27, v28, s19, v229
	v_med3_f32 v26, v26, s19, v229
	v_cvt_pk_fp8_f32 v30, v27, v26 op_sel:[0,0,1]
	v_mul_f32_e32 v31, v90, v24
	v_mul_f32_e32 v41, v91, v24
	v_mul_f32_e32 v42, v92, v24
	global_store_dword v25, v30, s[10:11] offset:120
	global_load_dwordx4 v[172:175], v[2:3], off offset:832
	v_mov_b32_e32 v30, v1
	v_mul_f32_e32 v43, v93, v24
	s_waitcnt vmcnt(20)
	v_mul_f32_e32 v26, v31, v180
	v_mul_f32_e32 v27, v41, v181
	v_med3_f32 v26, v26, s19, v229
	v_med3_f32 v27, v27, s19, v229
	v_cvt_pk_fp8_f32 v30, v26, v27
	v_mul_f32_e32 v28, v42, v182
	v_mul_f32_e32 v26, v43, v183
	v_med3_f32 v27, v28, s19, v229
	v_med3_f32 v26, v26, s19, v229
	v_cvt_pk_fp8_f32 v30, v27, v26 op_sel:[0,0,1]
	v_mul_f32_e32 v31, v80, v24
	v_mul_f32_e32 v41, v81, v24
	v_mul_f32_e32 v42, v82, v24
	global_store_dword v25, v30, s[10:11] offset:128
	global_load_dwordx4 v[180:183], v[2:3], off offset:864
	v_mov_b32_e32 v30, v1
	v_mul_f32_e32 v43, v83, v24
	s_waitcnt vmcnt(20)
	v_mul_f32_e32 v26, v31, v184
	v_mul_f32_e32 v27, v41, v185
	v_med3_f32 v26, v26, s19, v229
	v_med3_f32 v27, v27, s19, v229
	v_cvt_pk_fp8_f32 v30, v26, v27
	v_mul_f32_e32 v28, v42, v186
	v_mul_f32_e32 v26, v43, v187
	v_med3_f32 v27, v28, s19, v229
	v_med3_f32 v26, v26, s19, v229
	v_cvt_pk_fp8_f32 v30, v27, v26 op_sel:[0,0,1]
	v_mul_f32_e32 v31, v84, v24
	v_mul_f32_e32 v41, v85, v24
	v_mul_f32_e32 v42, v74, v24
	global_store_dword v25, v30, s[10:11] offset:136
	global_load_dwordx4 v[184:187], v[2:3], off offset:896
	v_mov_b32_e32 v30, v1
	v_mul_f32_e32 v43, v75, v24
	s_waitcnt vmcnt(20)
	v_mul_f32_e32 v26, v31, v188
	v_mul_f32_e32 v27, v41, v189
	v_med3_f32 v26, v26, s19, v229
	v_med3_f32 v27, v27, s19, v229
	v_cvt_pk_fp8_f32 v30, v26, v27
	v_mul_f32_e32 v28, v42, v190
	v_mul_f32_e32 v26, v43, v191
	v_med3_f32 v27, v28, s19, v229
	v_med3_f32 v26, v26, s19, v229
	v_cvt_pk_fp8_f32 v30, v27, v26 op_sel:[0,0,1]
	v_mul_f32_e32 v31, v66, v24
	v_mul_f32_e32 v41, v67, v24
	v_mul_f32_e32 v42, v68, v24
	global_store_dword v25, v30, s[10:11] offset:144
	global_load_dwordx4 v[188:191], v[2:3], off offset:928
	v_mov_b32_e32 v30, v1
	v_mul_f32_e32 v43, v69, v24
	s_waitcnt vmcnt(20)
	v_mul_f32_e32 v26, v31, v192
	v_mul_f32_e32 v27, v41, v193
	v_med3_f32 v26, v26, s19, v229
	v_med3_f32 v27, v27, s19, v229
	v_cvt_pk_fp8_f32 v30, v26, v27
	v_mul_f32_e32 v28, v42, v194
	v_mul_f32_e32 v26, v43, v195
	v_med3_f32 v27, v28, s19, v229
	v_med3_f32 v26, v26, s19, v229
	v_cvt_pk_fp8_f32 v30, v27, v26 op_sel:[0,0,1]
	v_mul_f32_e32 v31, v70, v24
	v_mul_f32_e32 v41, v71, v24
	v_mul_f32_e32 v42, v72, v24
	global_store_dword v25, v30, s[10:11] offset:152
	global_load_dwordx4 v[192:195], v[2:3], off offset:960
	v_mov_b32_e32 v30, v1
	v_mul_f32_e32 v43, v73, v24
	s_waitcnt vmcnt(20)
	v_mul_f32_e32 v26, v31, v196
	v_mul_f32_e32 v27, v41, v197
	v_med3_f32 v26, v26, s19, v229
	v_med3_f32 v27, v27, s19, v229
	v_cvt_pk_fp8_f32 v30, v26, v27
	v_mul_f32_e32 v28, v42, v198
	v_mul_f32_e32 v26, v43, v199
	v_med3_f32 v27, v28, s19, v229
	v_med3_f32 v26, v26, s19, v229
	v_cvt_pk_fp8_f32 v30, v27, v26 op_sel:[0,0,1]
	v_mul_f32_e32 v31, v64, v24
	v_mul_f32_e32 v41, v65, v24
	v_mul_f32_e32 v42, v54, v24
	global_store_dword v25, v30, s[10:11] offset:160
	global_load_dwordx4 v[196:199], v[2:3], off offset:992
	v_mov_b32_e32 v30, v1
	v_mul_f32_e32 v43, v55, v24
	s_waitcnt vmcnt(20)
	v_mul_f32_e32 v26, v31, v200
	v_mul_f32_e32 v27, v41, v201
	v_med3_f32 v26, v26, s19, v229
	v_med3_f32 v27, v27, s19, v229
	v_cvt_pk_fp8_f32 v30, v26, v27
	v_mul_f32_e32 v28, v42, v202
	v_mul_f32_e32 v26, v43, v203
	v_med3_f32 v27, v28, s19, v229
	v_med3_f32 v26, v26, s19, v229
	v_cvt_pk_fp8_f32 v30, v27, v26 op_sel:[0,0,1]
	v_mul_f32_e32 v31, v56, v24
	v_mul_f32_e32 v41, v57, v24
	v_mul_f32_e32 v42, v58, v24
	global_store_dword v25, v30, s[10:11] offset:168
	v_mov_b32_e32 v30, v1
	v_mul_f32_e32 v43, v59, v24
	s_waitcnt vmcnt(19)
	v_mul_f32_e32 v26, v31, v204
	v_mul_f32_e32 v27, v41, v205
	v_med3_f32 v26, v26, s19, v229
	v_med3_f32 v27, v27, s19, v229
	v_cvt_pk_fp8_f32 v30, v26, v27
	v_mul_f32_e32 v28, v42, v206
	v_mul_f32_e32 v26, v43, v207
	v_med3_f32 v27, v28, s19, v229
	v_med3_f32 v26, v26, s19, v229
	v_cvt_pk_fp8_f32 v30, v27, v26 op_sel:[0,0,1]
	v_mul_f32_e32 v31, v48, v24
	v_mul_f32_e32 v41, v49, v24
	v_mul_f32_e32 v42, v50, v24
	global_store_dword v25, v30, s[10:11] offset:176
	v_mov_b32_e32 v30, v1
	v_mul_f32_e32 v43, v51, v24
	s_waitcnt vmcnt(18)
	v_mul_f32_e32 v26, v31, v160
	v_mul_f32_e32 v27, v41, v161
	v_med3_f32 v26, v26, s19, v229
	v_med3_f32 v27, v27, s19, v229
	v_cvt_pk_fp8_f32 v30, v26, v27
	v_mul_f32_e32 v28, v42, v162
	v_mul_f32_e32 v26, v43, v163
	v_med3_f32 v27, v28, s19, v229
	v_med3_f32 v26, v26, s19, v229
	v_cvt_pk_fp8_f32 v30, v27, v26 op_sel:[0,0,1]
	v_mul_f32_e32 v31, v52, v24
	v_mul_f32_e32 v41, v53, v24
	global_store_dword v25, v30, s[10:11] offset:184
	v_mov_b32_e32 v30, v1
	s_waitcnt vmcnt(17)
	v_mul_f32_e32 v26, v31, v164
	v_mul_f32_e32 v27, v41, v165
	v_med3_f32 v26, v26, s19, v229
	v_med3_f32 v27, v27, s19, v229
	v_cvt_pk_fp8_f32 v30, v26, v27
	v_mul_f32_e32 v28, v34, v166
	v_mul_f32_e32 v26, v35, v167
	v_med3_f32 v27, v28, s19, v229
	v_med3_f32 v26, v26, s19, v229
	v_cvt_pk_fp8_f32 v30, v27, v26 op_sel:[0,0,1]
	global_store_dword v25, v30, s[10:11] offset:192
	v_mov_b32_e32 v30, v1
	s_waitcnt vmcnt(16)
	v_mul_f32_e32 v10, v10, v168
	v_mul_f32_e32 v11, v11, v169
	v_med3_f32 v10, v10, s19, v229
	v_med3_f32 v11, v11, s19, v229
	v_cvt_pk_fp8_f32 v30, v10, v11
	v_mul_f32_e32 v12, v12, v170
	v_mul_f32_e32 v10, v13, v171
	v_med3_f32 v11, v12, s19, v229
	v_med3_f32 v10, v10, s19, v229
	v_cvt_pk_fp8_f32 v30, v11, v10 op_sel:[0,0,1]
	v_mov_b32_e32 v26, v1
	v_mul_f32_e32 v27, v32, v24
	v_mul_f32_e32 v28, v33, v24
	global_store_dword v25, v30, s[10:11] offset:200
	s_waitcnt vmcnt(15)
	v_mul_f32_e32 v10, v14, v172
	v_mul_f32_e32 v11, v15, v173
	v_med3_f32 v10, v10, s19, v229
	v_med3_f32 v11, v11, s19, v229
	v_cvt_pk_fp8_f32 v26, v10, v11
	v_mul_f32_e32 v12, v27, v174
	v_mul_f32_e32 v10, v28, v175
	v_med3_f32 v11, v12, s19, v229
	v_med3_f32 v10, v10, s19, v229
	v_cvt_pk_fp8_f32 v26, v11, v10 op_sel:[0,0,1]
	v_mov_b32_e32 v14, v1
	global_store_dword v25, v26, s[10:11] offset:208
	s_waitcnt vmcnt(14)
	v_mul_f32_e32 v4, v4, v180
	v_mul_f32_e32 v5, v5, v181
	v_med3_f32 v4, v4, s19, v229
	v_med3_f32 v5, v5, s19, v229
	v_cvt_pk_fp8_f32 v14, v4, v5
	v_mul_f32_e32 v6, v6, v182
	v_mul_f32_e32 v4, v7, v183
	v_med3_f32 v5, v6, s19, v229
	v_med3_f32 v4, v4, s19, v229
	v_cvt_pk_fp8_f32 v14, v5, v4 op_sel:[0,0,1]
	v_mov_b32_e32 v10, v1
	v_mul_f32_e32 v11, v39, v24
	v_mul_f32_e32 v12, v40, v24
	global_store_dword v25, v14, s[10:11] offset:216
	s_waitcnt vmcnt(13)
	v_mul_f32_e32 v4, v8, v184
	v_mul_f32_e32 v5, v9, v185
	v_med3_f32 v4, v4, s19, v229
	v_med3_f32 v5, v5, s19, v229
	v_cvt_pk_fp8_f32 v10, v4, v5
	v_mul_f32_e32 v6, v11, v186
	v_mul_f32_e32 v4, v12, v187
	v_med3_f32 v5, v6, s19, v229
	v_med3_f32 v4, v4, s19, v229
	v_cvt_pk_fp8_f32 v10, v5, v4 op_sel:[0,0,1]
	v_mul_f32_e32 v9, v36, v24
	v_mov_b32_e32 v8, v1
	v_mul_f32_e32 v11, v38, v24
	global_store_dword v25, v10, s[10:11] offset:224
	v_mul_f32_e32 v10, v37, v24
	v_mul_f32_e32 v12, v23, v24
	s_waitcnt vmcnt(12)
	v_mul_f32_e32 v4, v9, v188
	v_mul_f32_e32 v5, v10, v189
	v_med3_f32 v4, v4, s19, v229
	v_med3_f32 v5, v5, s19, v229
	v_cvt_pk_fp8_f32 v8, v4, v5
	v_mul_f32_e32 v6, v11, v190
	v_mul_f32_e32 v4, v12, v191
	v_med3_f32 v5, v6, s19, v229
	v_med3_f32 v4, v4, s19, v229
	v_cvt_pk_fp8_f32 v8, v5, v4 op_sel:[0,0,1]
	v_mul_f32_e32 v9, v19, v24
	v_mul_f32_e32 v10, v20, v24
	v_mul_f32_e32 v11, v21, v24
	global_store_dword v25, v8, s[10:11] offset:232
	v_mov_b32_e32 v8, v1
	v_mul_f32_e32 v12, v22, v24
	s_waitcnt vmcnt(11)
	v_mul_f32_e32 v4, v9, v192
	v_mul_f32_e32 v5, v10, v193
	v_med3_f32 v4, v4, s19, v229
	v_med3_f32 v5, v5, s19, v229
	v_cvt_pk_fp8_f32 v8, v4, v5
	v_mul_f32_e32 v6, v11, v194
	v_mul_f32_e32 v4, v12, v195
	v_med3_f32 v5, v6, s19, v229
	v_med3_f32 v4, v4, s19, v229
	v_cvt_pk_fp8_f32 v8, v5, v4 op_sel:[0,0,1]
	v_mul_f32_e32 v6, v16, v24
	v_mul_f32_e32 v7, v17, v24
	global_store_dword v25, v8, s[10:11] offset:240
	v_mul_f32_e32 v8, v18, v24
	s_waitcnt vmcnt(10)
	v_mul_f32_e32 v2, v6, v196
	v_mul_f32_e32 v3, v7, v197
	v_med3_f32 v2, v2, s19, v229
	v_med3_f32 v3, v3, s19, v229
	v_mov_b32_e32 v6, v1
	v_cvt_pk_fp8_f32 v6, v2, v3
	v_mul_f32_e32 v4, v8, v198
	v_mul_f32_e32 v0, v0, v199
	v_med3_f32 v2, v4, s19, v229
	v_med3_f32 v0, v0, s19, v229
	v_cvt_pk_fp8_f32 v6, v2, v0 op_sel:[0,0,1]
	global_store_dword v25, v6, s[10:11] offset:248
	s_branch .LBB0_260

.LBB0_529:
	s_or_b64 exec, exec, s[38:39]
	v_readlane_b32 s12, v253, 42
	s_waitcnt lgkmcnt(0)
	s_barrier
	v_lshl_add_u32 v3, v86, 2, s12
	ds_read_b32 v2, v85 offset:4352
	ds_read_b32 v3, v3 offset:4864
	s_movk_i32 s12, 0xc00
	v_lshl_add_u32 v35, s87, 8, v82
	v_mov_b32_e32 v62, v1
	v_mov_b32_e32 v63, v1
	s_waitcnt lgkmcnt(0)
	v_add_f32_e32 v2, v2, v3
	v_fmamk_f32 v2, v2, 0x3b800000, v210
	v_rsq_f32_e32 v34, v2
	v_mov_b64_e32 v[2:3], s[10:11]
	v_mad_u64_u32 v[2:3], s[20:21], v73, s12, v[2:3]
	v_mov_b32_e32 v4, v3
	v_mad_u64_u32 v[4:5], s[20:21], v72, s12, v[4:5]
	v_readlane_b32 s12, v253, 51
	v_mov_b32_e32 v3, v4
	v_mul_f32_e32 v43, v78, v34
	v_add_u32_e32 v6, s12, v35
	v_ashrrev_i32_e32 v7, 31, v6
	v_lshl_add_u64 v[4:5], v[6:7], 2, s[72:73]
	global_load_dwordx4 v[68:71], v[4:5], off
	v_readlane_b32 s101, v253, 53
	s_nop 1
	v_add_u32_e32 v182, s101, v35
	v_ashrrev_i32_e32 v183, 31, v182
	v_lshl_add_u64 v[232:233], v[182:183], 2, s[72:73]
	global_load_dwordx4 v[190:193], v[4:5], off offset:32
	global_load_dwordx4 v[194:197], v[4:5], off offset:64
	global_load_dwordx4 v[198:201], v[4:5], off offset:96
	global_load_dwordx4 v[202:205], v[4:5], off offset:128
	global_load_dwordx4 v[206:209], v[4:5], off offset:160
	global_load_dwordx4 v[212:215], v[4:5], off offset:192
	global_load_dwordx4 v[216:219], v[4:5], off offset:224
	global_load_dwordx4 v[220:223], v[232:233], off
	global_load_dwordx4 v[224:227], v[232:233], off offset:32
	global_load_dwordx4 v[240:243], v[232:233], off offset:64
	global_load_dwordx4 v[244:247], v[232:233], off offset:96
	v_mul_f32_e32 v44, v80, v34
	v_mul_f32_e32 v45, v83, v34
	v_mul_f32_e32 v46, v88, v34
	s_mov_b64 s[20:21], 0x48200800
	v_lshl_add_u64 v[2:3], v[2:3], 0, s[20:21]
	v_mul_f32_e32 v0, v0, v34
	v_readlane_b32 s12, v253, 53
	v_mul_f32_e32 v8, v8, v34
	v_mul_f32_e32 v9, v9, v34
	s_add_i32 s84, s84, s70
	s_cmpk_lt_i32 s84, 0x200
	s_waitcnt vmcnt(11)
	v_mul_f32_e32 v43, v68, v43
	v_mul_f32_e32 v44, v69, v44
	v_med3_f32 v43, v43, s19, v229
	v_med3_f32 v44, v44, s19, v229
	v_cvt_pk_fp8_f32 v62, v43, v44
	v_mul_f32_e32 v45, v70, v45
	v_mul_f32_e32 v46, v71, v46
	v_med3_f32 v43, v45, s19, v229
	v_med3_f32 v44, v46, s19, v229
	v_cvt_pk_fp8_f32 v62, v43, v44 op_sel:[0,0,1]
	v_lshl_add_u64 v[44:45], v[2:3], 0, v[6:7]
	v_mul_f32_e32 v7, v79, v34
	v_mul_f32_e32 v43, v81, v34
	global_store_dword v[44:45], v62, off
	v_mul_f32_e32 v46, v84, v34
	v_mul_f32_e32 v62, v89, v34
	v_add_u32_e32 v44, 8, v6
	v_ashrrev_i32_e32 v45, 31, v44
	v_lshl_add_u64 v[44:45], v[2:3], 0, v[44:45]
	s_waitcnt vmcnt(11)
	v_mul_f32_e32 v7, v7, v190
	v_mul_f32_e32 v43, v43, v191
	v_med3_f32 v7, v7, s19, v229
	v_med3_f32 v43, v43, s19, v229
	v_cvt_pk_fp8_f32 v63, v7, v43
	v_mul_f32_e32 v46, v46, v192
	v_mul_f32_e32 v62, v62, v193
	v_med3_f32 v7, v46, s19, v229
	v_med3_f32 v43, v62, s19, v229
	v_cvt_pk_fp8_f32 v63, v7, v43 op_sel:[0,0,1]
	v_mul_f32_e32 v7, v74, v34
	v_mul_f32_e32 v43, v75, v34
	v_mul_f32_e32 v46, v76, v34
	global_store_dword v[44:45], v63, off
	global_load_dwordx4 v[190:193], v[232:233], off offset:128
	v_mov_b32_e32 v63, v1
	v_mul_f32_e32 v62, v77, v34
	v_add_u32_e32 v44, 16, v6
	v_ashrrev_i32_e32 v45, 31, v44
	v_lshl_add_u64 v[44:45], v[2:3], 0, v[44:45]
	s_waitcnt vmcnt(12)
	v_mul_f32_e32 v7, v7, v194
	v_mul_f32_e32 v43, v43, v195
	v_med3_f32 v7, v7, s19, v229
	v_med3_f32 v43, v43, s19, v229
	v_cvt_pk_fp8_f32 v63, v7, v43
	v_mul_f32_e32 v46, v46, v196
	v_mul_f32_e32 v62, v62, v197
	v_med3_f32 v7, v46, s19, v229
	v_med3_f32 v43, v62, s19, v229
	v_cvt_pk_fp8_f32 v63, v7, v43 op_sel:[0,0,1]
	v_mul_f32_e32 v7, v58, v34
	v_mul_f32_e32 v43, v59, v34
	v_mov_b32_e32 v59, v1
	global_store_dword v[44:45], v63, off
	global_load_dwordx4 v[194:197], v[232:233], off offset:160
	v_mul_f32_e32 v46, v60, v34
	v_mul_f32_e32 v58, v61, v34
	v_add_u32_e32 v44, 24, v6
	v_ashrrev_i32_e32 v45, 31, v44
	v_lshl_add_u64 v[44:45], v[2:3], 0, v[44:45]
	s_waitcnt vmcnt(13)
	v_mul_f32_e32 v7, v7, v198
	v_mul_f32_e32 v43, v43, v199
	v_med3_f32 v7, v7, s19, v229
	v_med3_f32 v43, v43, s19, v229
	v_cvt_pk_fp8_f32 v59, v7, v43
	v_mul_f32_e32 v46, v46, v200
	v_mul_f32_e32 v58, v58, v201
	v_med3_f32 v7, v46, s19, v229
	v_med3_f32 v43, v58, s19, v229
	v_cvt_pk_fp8_f32 v59, v7, v43 op_sel:[0,0,1]
	v_mul_f32_e32 v7, v54, v34
	v_mul_f32_e32 v43, v55, v34
	v_mov_b32_e32 v55, v1
	global_store_dword v[44:45], v59, off
	global_load_dwordx4 v[198:201], v[232:233], off offset:192
	v_mul_f32_e32 v46, v56, v34
	v_mul_f32_e32 v54, v57, v34
	v_add_u32_e32 v44, 32, v6
	v_ashrrev_i32_e32 v45, 31, v44
	v_lshl_add_u64 v[44:45], v[2:3], 0, v[44:45]
	s_waitcnt vmcnt(14)
	v_mul_f32_e32 v7, v7, v202
	v_mul_f32_e32 v43, v43, v203
	v_med3_f32 v7, v7, s19, v229
	v_med3_f32 v43, v43, s19, v229
	v_cvt_pk_fp8_f32 v55, v7, v43
	v_mul_f32_e32 v46, v46, v204
	v_mul_f32_e32 v54, v54, v205
	v_med3_f32 v7, v46, s19, v229
	v_med3_f32 v43, v54, s19, v229
	v_cvt_pk_fp8_f32 v55, v7, v43 op_sel:[0,0,1]
	v_mul_f32_e32 v7, v50, v34
	v_mul_f32_e32 v43, v51, v34
	v_mov_b32_e32 v51, v1
	global_store_dword v[44:45], v55, off
	global_load_dwordx4 v[202:205], v[232:233], off offset:224
	v_mul_f32_e32 v46, v52, v34
	v_mul_f32_e32 v50, v53, v34
	v_add_u32_e32 v44, 40, v6
	v_ashrrev_i32_e32 v45, 31, v44
	v_lshl_add_u64 v[44:45], v[2:3], 0, v[44:45]
	s_waitcnt vmcnt(15)
	v_mul_f32_e32 v7, v7, v206
	v_mul_f32_e32 v43, v43, v207
	v_med3_f32 v7, v7, s19, v229
	v_med3_f32 v43, v43, s19, v229
	v_cvt_pk_fp8_f32 v51, v7, v43
	v_mul_f32_e32 v46, v46, v208
	v_mul_f32_e32 v50, v50, v209
	v_med3_f32 v7, v46, s19, v229
	v_med3_f32 v43, v50, s19, v229
	v_cvt_pk_fp8_f32 v51, v7, v43 op_sel:[0,0,1]
	v_mul_f32_e32 v7, v39, v34
	v_mul_f32_e32 v39, v40, v34
	v_mul_f32_e32 v40, v41, v34
	global_store_dword v[44:45], v51, off
	v_mul_f32_e32 v41, v42, v34
	v_mov_b32_e32 v42, v1
	v_add_u32_e32 v44, 48, v6
	v_ashrrev_i32_e32 v45, 31, v44
	s_waitcnt vmcnt(15)
	v_mul_f32_e32 v7, v7, v212
	v_mul_f32_e32 v39, v39, v213
	v_med3_f32 v7, v7, s19, v229
	v_med3_f32 v39, v39, s19, v229
	v_cvt_pk_fp8_f32 v42, v7, v39
	v_mul_f32_e32 v40, v40, v214
	v_mul_f32_e32 v41, v41, v215
	v_med3_f32 v7, v40, s19, v229
	v_med3_f32 v39, v41, s19, v229
	v_cvt_pk_fp8_f32 v42, v7, v39 op_sel:[0,0,1]
	v_lshl_add_u64 v[40:41], v[2:3], 0, v[44:45]
	global_store_dword v[40:41], v42, off
	v_add_u32_e32 v40, 56, v6
	v_ashrrev_i32_e32 v41, 31, v40
	s_waitcnt vmcnt(15)
	v_mul_f32_e32 v0, v0, v216
	v_mul_f32_e32 v4, v36, v34
	v_mul_f32_e32 v4, v4, v217
	v_mul_f32_e32 v5, v37, v34
	v_mul_f32_e32 v5, v5, v218
	v_mul_f32_e32 v6, v38, v34
	v_mul_f32_e32 v6, v6, v219
	v_med3_f32 v0, v0, s19, v229
	v_med3_f32 v4, v4, s19, v229
	v_mov_b32_e32 v7, v1
	v_cvt_pk_fp8_f32 v7, v0, v4
	v_med3_f32 v0, v5, s19, v229
	v_med3_f32 v4, v6, s19, v229
	v_cvt_pk_fp8_f32 v7, v0, v4 op_sel:[0,0,1]
	v_lshl_add_u64 v[4:5], v[2:3], 0, v[40:41]
	v_mul_f32_e32 v0, v18, v34
	v_mul_f32_e32 v18, v19, v34
	global_store_dword v[4:5], v7, off
	v_add_u32_e32 v4, s12, v35
	v_ashrrev_i32_e32 v5, 31, v4
	v_lshl_add_u64 v[6:7], v[4:5], 2, s[72:73]
	v_mul_f32_e32 v19, v20, v34
	v_mul_f32_e32 v20, v21, v34
	v_mov_b32_e32 v21, v1
	s_waitcnt vmcnt(15)
	v_mul_f32_e32 v0, v0, v220
	v_mul_f32_e32 v18, v18, v221
	v_med3_f32 v0, v0, s19, v229
	v_med3_f32 v18, v18, s19, v229
	v_cvt_pk_fp8_f32 v21, v0, v18
	v_mul_f32_e32 v19, v19, v222
	v_mul_f32_e32 v20, v20, v223
	v_med3_f32 v0, v19, s19, v229
	v_med3_f32 v18, v20, s19, v229
	v_cvt_pk_fp8_f32 v21, v0, v18 op_sel:[0,0,1]
	v_lshl_add_u64 v[18:19], v[2:3], 0, v[4:5]
	v_mul_f32_e32 v0, v22, v34
	v_mul_f32_e32 v5, v23, v34
	global_store_dword v[18:19], v21, off
	v_add_u32_e32 v36, 8, v4
	v_ashrrev_i32_e32 v37, 31, v36
	v_add_u32_e32 v22, 16, v4
	v_ashrrev_i32_e32 v23, 31, v22
	s_waitcnt vmcnt(15)
	v_mul_f32_e32 v0, v0, v224
	v_mul_f32_e32 v5, v5, v225
	v_mul_f32_e32 v18, v24, v34
	v_mul_f32_e32 v18, v18, v226
	v_med3_f32 v0, v0, s19, v229
	v_med3_f32 v5, v5, s19, v229
	v_mov_b32_e32 v20, v1
	v_cvt_pk_fp8_f32 v20, v0, v5
	v_mul_f32_e32 v19, v25, v34
	v_mul_f32_e32 v19, v19, v227
	v_med3_f32 v0, v18, s19, v229
	v_med3_f32 v5, v19, s19, v229
	v_cvt_pk_fp8_f32 v20, v0, v5 op_sel:[0,0,1]
	v_lshl_add_u64 v[18:19], v[2:3], 0, v[36:37]
	v_mul_f32_e32 v0, v26, v34
	v_mul_f32_e32 v5, v27, v34
	global_store_dword v[18:19], v20, off
	s_waitcnt vmcnt(15)
	v_mul_f32_e32 v0, v0, v240
	v_mul_f32_e32 v5, v5, v241
	v_mul_f32_e32 v18, v28, v34
	v_mul_f32_e32 v18, v18, v242
	v_med3_f32 v0, v0, s19, v229
	v_med3_f32 v5, v5, s19, v229
	v_mov_b32_e32 v20, v1
	v_cvt_pk_fp8_f32 v20, v0, v5
	v_mul_f32_e32 v19, v29, v34
	v_mul_f32_e32 v19, v19, v243
	v_med3_f32 v0, v18, s19, v229
	v_med3_f32 v5, v19, s19, v229
	v_cvt_pk_fp8_f32 v20, v0, v5 op_sel:[0,0,1]
	v_lshl_add_u64 v[18:19], v[2:3], 0, v[22:23]
	v_mul_f32_e32 v0, v30, v34
	v_mul_f32_e32 v5, v31, v34
	global_store_dword v[18:19], v20, off
	v_add_u32_e32 v22, 24, v4
	v_ashrrev_i32_e32 v23, 31, v22
	s_waitcnt vmcnt(15)
	v_mul_f32_e32 v0, v0, v244
	v_mul_f32_e32 v5, v5, v245
	v_mul_f32_e32 v18, v32, v34
	v_mul_f32_e32 v18, v18, v246
	v_med3_f32 v0, v0, s19, v229
	v_med3_f32 v5, v5, s19, v229
	v_mov_b32_e32 v20, v1
	v_cvt_pk_fp8_f32 v20, v0, v5
	v_mul_f32_e32 v19, v33, v34
	v_mul_f32_e32 v19, v19, v247
	v_med3_f32 v0, v18, s19, v229
	v_med3_f32 v5, v19, s19, v229
	v_cvt_pk_fp8_f32 v20, v0, v5 op_sel:[0,0,1]
	v_lshl_add_u64 v[18:19], v[2:3], 0, v[22:23]
	v_mul_f32_e32 v0, v47, v34
	v_mul_f32_e32 v5, v48, v34
	global_store_dword v[18:19], v20, off
	v_add_u32_e32 v22, 32, v4
	v_ashrrev_i32_e32 v23, 31, v22
	s_waitcnt vmcnt(13)
	v_mul_f32_e32 v0, v0, v190
	v_mul_f32_e32 v5, v5, v191
	v_mul_f32_e32 v18, v49, v34
	v_mul_f32_e32 v18, v18, v192
	v_med3_f32 v0, v0, s19, v229
	v_med3_f32 v5, v5, s19, v229
	v_mov_b32_e32 v20, v1
	v_cvt_pk_fp8_f32 v20, v0, v5
	v_mul_f32_e32 v19, v66, v34
	v_mul_f32_e32 v19, v19, v193
	v_med3_f32 v0, v18, s19, v229
	v_med3_f32 v5, v19, s19, v229
	v_cvt_pk_fp8_f32 v20, v0, v5 op_sel:[0,0,1]
	v_lshl_add_u64 v[18:19], v[2:3], 0, v[22:23]
	v_mul_f32_e32 v0, v64, v34
	v_mul_f32_e32 v5, v65, v34
	global_store_dword v[18:19], v20, off
	v_add_u32_e32 v22, 40, v4
	v_ashrrev_i32_e32 v23, 31, v22
	s_waitcnt vmcnt(12)
	v_mul_f32_e32 v0, v0, v194
	v_mul_f32_e32 v5, v5, v195
	v_med3_f32 v0, v0, s19, v229
	v_med3_f32 v5, v5, s19, v229
	v_mov_b32_e32 v18, v1
	v_cvt_pk_fp8_f32 v18, v0, v5
	v_mul_f32_e32 v8, v8, v196
	v_mul_f32_e32 v9, v9, v197
	v_med3_f32 v0, v8, s19, v229
	v_med3_f32 v5, v9, s19, v229
	v_cvt_pk_fp8_f32 v18, v0, v5 op_sel:[0,0,1]
	v_lshl_add_u64 v[8:9], v[2:3], 0, v[22:23]
	v_mul_f32_e32 v0, v10, v34
	v_mul_f32_e32 v5, v11, v34
	global_store_dword v[8:9], v18, off
	v_mul_f32_e32 v10, v12, v34
	v_mov_b32_e32 v12, v1
	v_mul_f32_e32 v11, v13, v34
	v_add_u32_e32 v8, 48, v4
	v_ashrrev_i32_e32 v9, 31, v8
	v_lshl_add_u64 v[8:9], v[2:3], 0, v[8:9]
	s_waitcnt vmcnt(11)
	v_mul_f32_e32 v0, v0, v198
	v_mul_f32_e32 v5, v5, v199
	v_med3_f32 v0, v0, s19, v229
	v_med3_f32 v5, v5, s19, v229
	v_cvt_pk_fp8_f32 v12, v0, v5
	v_mul_f32_e32 v10, v10, v200
	v_mul_f32_e32 v11, v11, v201
	v_med3_f32 v0, v10, s19, v229
	v_med3_f32 v5, v11, s19, v229
	v_cvt_pk_fp8_f32 v12, v0, v5 op_sel:[0,0,1]
	v_mul_f32_e32 v0, v14, v34
	global_store_dword v[8:9], v12, off
	v_add_u32_e32 v8, 56, v4
	v_ashrrev_i32_e32 v9, 31, v8
	v_lshl_add_u64 v[2:3], v[2:3], 0, v[8:9]
	s_waitcnt vmcnt(10)
	v_mul_f32_e32 v0, v0, v202
	v_mul_f32_e32 v4, v15, v34
	v_mul_f32_e32 v4, v4, v203
	v_mul_f32_e32 v5, v16, v34
	v_mul_f32_e32 v5, v5, v204
	v_mul_f32_e32 v6, v17, v34
	v_mul_f32_e32 v6, v6, v205
	v_med3_f32 v0, v0, s19, v229
	v_med3_f32 v4, v4, s19, v229
	v_mov_b32_e32 v7, v1
	v_cvt_pk_fp8_f32 v7, v0, v4
	v_med3_f32 v0, v5, s19, v229
	v_med3_f32 v4, v6, s19, v229
	v_cvt_pk_fp8_f32 v7, v0, v4 op_sel:[0,0,1]
	global_store_dword v[2:3], v7, off
	s_cbranch_scc0 .LBB0_654

.LBB0_731:
	s_cmp_eq_u32 s88, 0
	s_cbranch_scc1 .LBB0_733
	v_lshl_add_u32 v0, s88, 11, v170
	s_nop 15
	s_nop 15
	global_load_dwordx4 v[152:155], v0, s[46:47]
	global_load_dwordx4 v[156:159], v0, s[46:47] offset:2048
	v_add_u32_e32 v204, 0x18000, v0
	global_load_dwordx4 v[160:163], v204, s[46:47]
	global_load_dwordx4 v[172:175], v204, s[46:47] offset:2048
	v_add_u32_e32 v204, 0x30000, v0
	global_load_dwordx4 v[176:179], v204, s[46:47]
	global_load_dwordx4 v[180:183], v204, s[46:47] offset:2048
	v_add_u32_e32 v204, 0x48000, v0
	global_load_dwordx4 v[184:187], v204, s[46:47]
	global_load_dwordx4 v[188:191], v204, s[46:47] offset:2048
	v_add_u32_e32 v204, 0xc0000, v0
	global_load_dwordx4 v[192:195], v204, s[46:47]
	global_load_dwordx4 v[196:199], v204, s[46:47] offset:2048
	v_add_u32_e32 v204, 0xd8000, v0
	global_load_dwordx4 v[200:203], v204, s[46:47]
	global_load_dwordx4 v[212:215], v204, s[46:47] offset:2048
	v_add_u32_e32 v204, 0xf0000, v0
	global_load_dwordx4 v[216:219], v204, s[46:47]
	global_load_dwordx4 v[240:243], v204, s[46:47] offset:2048
	s_waitcnt vmcnt(12)
	v_cvt_f32_ubyte1_e32 v17, v152
	v_cvt_f32_ubyte0_e32 v10, v156
	v_cvt_f32_ubyte1_e32 v11, v156
	v_rcp_iflag_f32_e32 v10, v10
	v_rcp_iflag_f32_e32 v11, v11
	v_cvt_f32_ubyte0_e32 v16, v152
	v_cvt_f32_ubyte3_e32 v15, v152
	v_cvt_f32_ubyte2_e32 v14, v152
	v_pk_mul_f32 v[10:11], v[10:11], v[16:17]
	v_cvt_f32_ubyte0_e32 v2, v157
	v_cvt_f32_ubyte2_e32 v12, v156
	v_cvt_f32_ubyte3_e32 v6, v156
	v_pk_mul_f32 v[142:143], v[142:143], v[10:11]
	v_rcp_iflag_f32_e32 v10, v2
	v_cvt_f32_ubyte1_e32 v2, v157
	v_rcp_iflag_f32_e32 v12, v12
	v_rcp_iflag_f32_e32 v13, v6
	v_rcp_iflag_f32_e32 v11, v2
	v_cvt_f32_ubyte2_e32 v2, v157
	v_rcp_iflag_f32_e32 v6, v2
	v_cvt_f32_ubyte3_e32 v2, v157
	v_rcp_iflag_f32_e32 v7, v2
	v_pk_mul_f32 v[12:13], v[12:13], v[14:15]
	v_cvt_f32_ubyte1_e32 v15, v153
	v_pk_mul_f32 v[144:145], v[144:145], v[12:13]
	v_cvt_f32_ubyte3_e32 v13, v153
	v_cvt_f32_ubyte2_e32 v12, v153
	v_cvt_f32_ubyte0_e32 v14, v153
	v_pk_mul_f32 v[2:3], v[10:11], v[14:15]
	v_pk_mul_f32 v[6:7], v[6:7], v[12:13]
	v_pk_mul_f32 v[138:139], v[138:139], v[2:3]
	v_pk_mul_f32 v[140:141], v[140:141], v[6:7]
	v_cvt_f32_ubyte0_e32 v2, v158
	v_cvt_f32_ubyte1_e32 v3, v158
	v_cvt_f32_ubyte2_e32 v6, v158
	v_cvt_f32_ubyte3_e32 v7, v158
	v_rcp_iflag_f32_e32 v2, v2
	v_rcp_iflag_f32_e32 v3, v3
	v_rcp_iflag_f32_e32 v6, v6
	v_rcp_iflag_f32_e32 v7, v7
	v_cvt_f32_ubyte3_e32 v11, v154
	v_cvt_f32_ubyte2_e32 v10, v154
	v_cvt_f32_ubyte1_e32 v13, v154
	v_cvt_f32_ubyte0_e32 v12, v154
	v_pk_mul_f32 v[2:3], v[2:3], v[12:13]
	v_pk_mul_f32 v[6:7], v[6:7], v[10:11]
	v_cvt_f32_ubyte2_e32 v4, v159
	v_pk_mul_f32 v[136:137], v[136:137], v[6:7]
	v_pk_mul_f32 v[134:135], v[134:135], v[2:3]
	v_cvt_f32_ubyte0_e32 v2, v159
	v_cvt_f32_ubyte1_e32 v3, v159
	v_rcp_iflag_f32_e32 v6, v4
	v_cvt_f32_ubyte3_e32 v4, v159
	v_rcp_iflag_f32_e32 v2, v2
	v_rcp_iflag_f32_e32 v3, v3
	v_rcp_iflag_f32_e32 v7, v4
	v_cvt_f32_ubyte3_e32 v9, v155
	v_cvt_f32_ubyte2_e32 v8, v155
	v_cvt_f32_ubyte1_e32 v11, v155
	v_cvt_f32_ubyte0_e32 v10, v155
	v_pk_mul_f32 v[2:3], v[2:3], v[10:11]
	v_pk_mul_f32 v[4:5], v[6:7], v[8:9]
	v_pk_mul_f32 v[130:131], v[130:131], v[2:3]
	v_pk_mul_f32 v[132:133], v[132:133], v[4:5]
	v_add_u32_e32 v204, 0x108000, v0
	global_load_dwordx4 v[152:155], v204, s[46:47]
	global_load_dwordx4 v[156:159], v204, s[46:47] offset:2048
	s_waitcnt vmcnt(12)
	v_cvt_f32_ubyte1_e32 v17, v160
	v_cvt_f32_ubyte0_e32 v10, v172
	v_cvt_f32_ubyte1_e32 v11, v172
	v_rcp_iflag_f32_e32 v10, v10
	v_rcp_iflag_f32_e32 v11, v11
	v_cvt_f32_ubyte0_e32 v16, v160
	v_cvt_f32_ubyte3_e32 v15, v160
	v_cvt_f32_ubyte2_e32 v14, v160
	v_pk_mul_f32 v[10:11], v[10:11], v[16:17]
	v_cvt_f32_ubyte0_e32 v2, v173
	v_cvt_f32_ubyte2_e32 v12, v172
	v_cvt_f32_ubyte3_e32 v6, v172
	v_pk_mul_f32 v[126:127], v[126:127], v[10:11]
	v_rcp_iflag_f32_e32 v10, v2
	v_cvt_f32_ubyte1_e32 v2, v173
	v_rcp_iflag_f32_e32 v12, v12
	v_rcp_iflag_f32_e32 v13, v6
	v_rcp_iflag_f32_e32 v11, v2
	v_cvt_f32_ubyte2_e32 v2, v173
	v_rcp_iflag_f32_e32 v6, v2
	v_cvt_f32_ubyte3_e32 v2, v173
	v_rcp_iflag_f32_e32 v7, v2
	v_pk_mul_f32 v[12:13], v[12:13], v[14:15]
	v_cvt_f32_ubyte1_e32 v15, v161
	v_pk_mul_f32 v[128:129], v[128:129], v[12:13]
	v_cvt_f32_ubyte3_e32 v13, v161
	v_cvt_f32_ubyte2_e32 v12, v161
	v_cvt_f32_ubyte0_e32 v14, v161
	v_pk_mul_f32 v[2:3], v[10:11], v[14:15]
	v_pk_mul_f32 v[6:7], v[6:7], v[12:13]
	v_pk_mul_f32 v[122:123], v[122:123], v[2:3]
	v_pk_mul_f32 v[124:125], v[124:125], v[6:7]
	v_cvt_f32_ubyte0_e32 v2, v174
	v_cvt_f32_ubyte1_e32 v3, v174
	v_cvt_f32_ubyte2_e32 v6, v174
	v_cvt_f32_ubyte3_e32 v7, v174
	v_rcp_iflag_f32_e32 v2, v2
	v_rcp_iflag_f32_e32 v3, v3
	v_rcp_iflag_f32_e32 v6, v6
	v_rcp_iflag_f32_e32 v7, v7
	v_cvt_f32_ubyte3_e32 v11, v162
	v_cvt_f32_ubyte2_e32 v10, v162
	v_cvt_f32_ubyte1_e32 v13, v162
	v_cvt_f32_ubyte0_e32 v12, v162
	v_pk_mul_f32 v[2:3], v[2:3], v[12:13]
	v_pk_mul_f32 v[6:7], v[6:7], v[10:11]
	v_cvt_f32_ubyte2_e32 v4, v175
	v_pk_mul_f32 v[120:121], v[120:121], v[6:7]
	v_pk_mul_f32 v[118:119], v[118:119], v[2:3]
	v_cvt_f32_ubyte0_e32 v2, v175
	v_cvt_f32_ubyte1_e32 v3, v175
	v_rcp_iflag_f32_e32 v6, v4
	v_cvt_f32_ubyte3_e32 v4, v175
	v_rcp_iflag_f32_e32 v2, v2
	v_rcp_iflag_f32_e32 v3, v3
	v_rcp_iflag_f32_e32 v7, v4
	v_cvt_f32_ubyte3_e32 v9, v163
	v_cvt_f32_ubyte2_e32 v8, v163
	v_cvt_f32_ubyte1_e32 v11, v163
	v_cvt_f32_ubyte0_e32 v10, v163
	v_pk_mul_f32 v[2:3], v[2:3], v[10:11]
	v_pk_mul_f32 v[4:5], v[6:7], v[8:9]
	v_pk_mul_f32 v[114:115], v[114:115], v[2:3]
	v_pk_mul_f32 v[116:117], v[116:117], v[4:5]
	s_waitcnt vmcnt(10)
	v_cvt_f32_ubyte1_e32 v17, v176
	v_cvt_f32_ubyte0_e32 v10, v180
	v_cvt_f32_ubyte1_e32 v11, v180
	v_rcp_iflag_f32_e32 v10, v10
	v_rcp_iflag_f32_e32 v11, v11
	v_cvt_f32_ubyte0_e32 v16, v176
	v_cvt_f32_ubyte3_e32 v15, v176
	v_cvt_f32_ubyte2_e32 v14, v176
	v_pk_mul_f32 v[10:11], v[10:11], v[16:17]
	v_cvt_f32_ubyte0_e32 v2, v181
	v_cvt_f32_ubyte2_e32 v12, v180
	v_cvt_f32_ubyte3_e32 v6, v180
	v_pk_mul_f32 v[110:111], v[110:111], v[10:11]
	v_rcp_iflag_f32_e32 v10, v2
	v_cvt_f32_ubyte1_e32 v2, v181
	v_rcp_iflag_f32_e32 v12, v12
	v_rcp_iflag_f32_e32 v13, v6
	v_rcp_iflag_f32_e32 v11, v2
	v_cvt_f32_ubyte2_e32 v2, v181
	v_rcp_iflag_f32_e32 v6, v2
	v_cvt_f32_ubyte3_e32 v2, v181
	v_rcp_iflag_f32_e32 v7, v2
	v_pk_mul_f32 v[12:13], v[12:13], v[14:15]
	v_cvt_f32_ubyte1_e32 v15, v177
	v_pk_mul_f32 v[112:113], v[112:113], v[12:13]
	v_cvt_f32_ubyte3_e32 v13, v177
	v_cvt_f32_ubyte2_e32 v12, v177
	v_cvt_f32_ubyte0_e32 v14, v177
	v_pk_mul_f32 v[2:3], v[10:11], v[14:15]
	v_pk_mul_f32 v[6:7], v[6:7], v[12:13]
	v_pk_mul_f32 v[106:107], v[106:107], v[2:3]
	v_pk_mul_f32 v[108:109], v[108:109], v[6:7]
	v_cvt_f32_ubyte0_e32 v2, v182
	v_cvt_f32_ubyte1_e32 v3, v182
	v_cvt_f32_ubyte2_e32 v6, v182
	v_cvt_f32_ubyte3_e32 v7, v182
	v_rcp_iflag_f32_e32 v2, v2
	v_rcp_iflag_f32_e32 v3, v3
	v_rcp_iflag_f32_e32 v6, v6
	v_rcp_iflag_f32_e32 v7, v7
	v_cvt_f32_ubyte3_e32 v11, v178
	v_cvt_f32_ubyte2_e32 v10, v178
	v_cvt_f32_ubyte1_e32 v13, v178
	v_cvt_f32_ubyte0_e32 v12, v178
	v_pk_mul_f32 v[2:3], v[2:3], v[12:13]
	v_pk_mul_f32 v[6:7], v[6:7], v[10:11]
	v_cvt_f32_ubyte2_e32 v4, v183
	v_pk_mul_f32 v[104:105], v[104:105], v[6:7]
	v_pk_mul_f32 v[102:103], v[102:103], v[2:3]
	v_cvt_f32_ubyte0_e32 v2, v183
	v_cvt_f32_ubyte1_e32 v3, v183
	v_rcp_iflag_f32_e32 v6, v4
	v_cvt_f32_ubyte3_e32 v4, v183
	v_rcp_iflag_f32_e32 v2, v2
	v_rcp_iflag_f32_e32 v3, v3
	v_rcp_iflag_f32_e32 v7, v4
	v_cvt_f32_ubyte3_e32 v9, v179
	v_cvt_f32_ubyte2_e32 v8, v179
	v_cvt_f32_ubyte1_e32 v11, v179
	v_cvt_f32_ubyte0_e32 v10, v179
	v_pk_mul_f32 v[2:3], v[2:3], v[10:11]
	v_pk_mul_f32 v[4:5], v[6:7], v[8:9]
	v_pk_mul_f32 v[98:99], v[98:99], v[2:3]
	v_pk_mul_f32 v[100:101], v[100:101], v[4:5]
	s_waitcnt vmcnt(8)
	v_cvt_f32_ubyte1_e32 v17, v184
	v_cvt_f32_ubyte0_e32 v10, v188
	v_cvt_f32_ubyte1_e32 v11, v188
	v_rcp_iflag_f32_e32 v10, v10
	v_rcp_iflag_f32_e32 v11, v11
	v_cvt_f32_ubyte0_e32 v16, v184
	v_cvt_f32_ubyte3_e32 v15, v184
	v_cvt_f32_ubyte2_e32 v14, v184
	v_pk_mul_f32 v[10:11], v[10:11], v[16:17]
	v_cvt_f32_ubyte0_e32 v2, v189
	v_cvt_f32_ubyte2_e32 v12, v188
	v_cvt_f32_ubyte3_e32 v6, v188
	v_pk_mul_f32 v[94:95], v[94:95], v[10:11]
	v_rcp_iflag_f32_e32 v10, v2
	v_cvt_f32_ubyte1_e32 v2, v189
	v_rcp_iflag_f32_e32 v12, v12
	v_rcp_iflag_f32_e32 v13, v6
	v_rcp_iflag_f32_e32 v11, v2
	v_cvt_f32_ubyte2_e32 v2, v189
	v_rcp_iflag_f32_e32 v6, v2
	v_cvt_f32_ubyte3_e32 v2, v189
	v_rcp_iflag_f32_e32 v7, v2
	v_pk_mul_f32 v[12:13], v[12:13], v[14:15]
	v_cvt_f32_ubyte1_e32 v15, v185
	v_pk_mul_f32 v[96:97], v[96:97], v[12:13]
	v_cvt_f32_ubyte3_e32 v13, v185
	v_cvt_f32_ubyte2_e32 v12, v185
	v_cvt_f32_ubyte0_e32 v14, v185
	v_pk_mul_f32 v[2:3], v[10:11], v[14:15]
	v_pk_mul_f32 v[6:7], v[6:7], v[12:13]
	v_pk_mul_f32 v[90:91], v[90:91], v[2:3]
	v_pk_mul_f32 v[92:93], v[92:93], v[6:7]
	v_cvt_f32_ubyte0_e32 v2, v190
	v_cvt_f32_ubyte1_e32 v3, v190
	v_cvt_f32_ubyte2_e32 v6, v190
	v_cvt_f32_ubyte3_e32 v7, v190
	v_rcp_iflag_f32_e32 v2, v2
	v_rcp_iflag_f32_e32 v3, v3
	v_rcp_iflag_f32_e32 v6, v6
	v_rcp_iflag_f32_e32 v7, v7
	v_cvt_f32_ubyte3_e32 v11, v186
	v_cvt_f32_ubyte2_e32 v10, v186
	v_cvt_f32_ubyte1_e32 v13, v186
	v_cvt_f32_ubyte0_e32 v12, v186
	v_pk_mul_f32 v[2:3], v[2:3], v[12:13]
	v_pk_mul_f32 v[6:7], v[6:7], v[10:11]
	v_cvt_f32_ubyte2_e32 v4, v191
	v_pk_mul_f32 v[88:89], v[88:89], v[6:7]
	v_pk_mul_f32 v[86:87], v[86:87], v[2:3]
	v_cvt_f32_ubyte0_e32 v2, v191
	v_cvt_f32_ubyte1_e32 v3, v191
	v_rcp_iflag_f32_e32 v6, v4
	v_cvt_f32_ubyte3_e32 v4, v191
	v_rcp_iflag_f32_e32 v2, v2
	v_rcp_iflag_f32_e32 v3, v3
	v_rcp_iflag_f32_e32 v7, v4
	v_cvt_f32_ubyte3_e32 v9, v187
	v_cvt_f32_ubyte2_e32 v8, v187
	v_cvt_f32_ubyte1_e32 v11, v187
	v_cvt_f32_ubyte0_e32 v10, v187
	v_pk_mul_f32 v[2:3], v[2:3], v[10:11]
	v_pk_mul_f32 v[4:5], v[6:7], v[8:9]
	v_pk_mul_f32 v[82:83], v[82:83], v[2:3]
	v_pk_mul_f32 v[84:85], v[84:85], v[4:5]
	s_waitcnt vmcnt(6)
	v_cvt_f32_ubyte1_e32 v17, v192
	v_cvt_f32_ubyte0_e32 v10, v196
	v_cvt_f32_ubyte1_e32 v11, v196
	v_rcp_iflag_f32_e32 v10, v10
	v_rcp_iflag_f32_e32 v11, v11
	v_cvt_f32_ubyte0_e32 v16, v192
	v_cvt_f32_ubyte3_e32 v15, v192
	v_cvt_f32_ubyte2_e32 v14, v192
	v_pk_mul_f32 v[10:11], v[10:11], v[16:17]
	v_cvt_f32_ubyte0_e32 v2, v197
	v_cvt_f32_ubyte2_e32 v12, v196
	v_cvt_f32_ubyte3_e32 v6, v196
	v_pk_mul_f32 v[78:79], v[78:79], v[10:11]
	v_rcp_iflag_f32_e32 v10, v2
	v_cvt_f32_ubyte1_e32 v2, v197
	v_rcp_iflag_f32_e32 v12, v12
	v_rcp_iflag_f32_e32 v13, v6
	v_rcp_iflag_f32_e32 v11, v2
	v_cvt_f32_ubyte2_e32 v2, v197
	v_rcp_iflag_f32_e32 v6, v2
	v_cvt_f32_ubyte3_e32 v2, v197
	v_rcp_iflag_f32_e32 v7, v2
	v_pk_mul_f32 v[12:13], v[12:13], v[14:15]
	v_cvt_f32_ubyte1_e32 v15, v193
	v_pk_mul_f32 v[80:81], v[80:81], v[12:13]
	v_cvt_f32_ubyte3_e32 v13, v193
	v_cvt_f32_ubyte2_e32 v12, v193
	v_cvt_f32_ubyte0_e32 v14, v193
	v_pk_mul_f32 v[2:3], v[10:11], v[14:15]
	v_pk_mul_f32 v[6:7], v[6:7], v[12:13]
	v_pk_mul_f32 v[74:75], v[74:75], v[2:3]
	v_pk_mul_f32 v[76:77], v[76:77], v[6:7]
	v_cvt_f32_ubyte0_e32 v2, v198
	v_cvt_f32_ubyte1_e32 v3, v198
	v_cvt_f32_ubyte2_e32 v6, v198
	v_cvt_f32_ubyte3_e32 v7, v198
	v_rcp_iflag_f32_e32 v2, v2
	v_rcp_iflag_f32_e32 v3, v3
	v_rcp_iflag_f32_e32 v6, v6
	v_rcp_iflag_f32_e32 v7, v7
	v_cvt_f32_ubyte3_e32 v11, v194
	v_cvt_f32_ubyte2_e32 v10, v194
	v_cvt_f32_ubyte1_e32 v13, v194
	v_cvt_f32_ubyte0_e32 v12, v194
	v_pk_mul_f32 v[2:3], v[2:3], v[12:13]
	v_pk_mul_f32 v[6:7], v[6:7], v[10:11]
	v_cvt_f32_ubyte2_e32 v4, v199
	v_pk_mul_f32 v[72:73], v[72:73], v[6:7]
	v_pk_mul_f32 v[70:71], v[70:71], v[2:3]
	v_cvt_f32_ubyte0_e32 v2, v199
	v_cvt_f32_ubyte1_e32 v3, v199
	v_rcp_iflag_f32_e32 v6, v4
	v_cvt_f32_ubyte3_e32 v4, v199
	v_rcp_iflag_f32_e32 v2, v2
	v_rcp_iflag_f32_e32 v3, v3
	v_rcp_iflag_f32_e32 v7, v4
	v_cvt_f32_ubyte3_e32 v9, v195
	v_cvt_f32_ubyte2_e32 v8, v195
	v_cvt_f32_ubyte1_e32 v11, v195
	v_cvt_f32_ubyte0_e32 v10, v195
	v_pk_mul_f32 v[2:3], v[2:3], v[10:11]
	v_pk_mul_f32 v[4:5], v[6:7], v[8:9]
	v_pk_mul_f32 v[66:67], v[66:67], v[2:3]
	v_pk_mul_f32 v[68:69], v[68:69], v[4:5]
	s_waitcnt vmcnt(4)
	v_cvt_f32_ubyte1_e32 v17, v200
	v_cvt_f32_ubyte0_e32 v10, v212
	v_cvt_f32_ubyte1_e32 v11, v212
	v_rcp_iflag_f32_e32 v10, v10
	v_rcp_iflag_f32_e32 v11, v11
	v_cvt_f32_ubyte0_e32 v16, v200
	v_cvt_f32_ubyte3_e32 v15, v200
	v_cvt_f32_ubyte2_e32 v14, v200
	v_pk_mul_f32 v[10:11], v[10:11], v[16:17]
	v_cvt_f32_ubyte0_e32 v2, v213
	v_cvt_f32_ubyte2_e32 v12, v212
	v_cvt_f32_ubyte3_e32 v6, v212
	v_pk_mul_f32 v[62:63], v[62:63], v[10:11]
	v_rcp_iflag_f32_e32 v10, v2
	v_cvt_f32_ubyte1_e32 v2, v213
	v_rcp_iflag_f32_e32 v12, v12
	v_rcp_iflag_f32_e32 v13, v6
	v_rcp_iflag_f32_e32 v11, v2
	v_cvt_f32_ubyte2_e32 v2, v213
	v_rcp_iflag_f32_e32 v6, v2
	v_cvt_f32_ubyte3_e32 v2, v213
	v_rcp_iflag_f32_e32 v7, v2
	v_pk_mul_f32 v[12:13], v[12:13], v[14:15]
	v_cvt_f32_ubyte1_e32 v15, v201
	v_pk_mul_f32 v[64:65], v[64:65], v[12:13]
	v_cvt_f32_ubyte3_e32 v13, v201
	v_cvt_f32_ubyte2_e32 v12, v201
	v_cvt_f32_ubyte0_e32 v14, v201
	v_pk_mul_f32 v[2:3], v[10:11], v[14:15]
	v_pk_mul_f32 v[6:7], v[6:7], v[12:13]
	v_pk_mul_f32 v[58:59], v[58:59], v[2:3]
	v_pk_mul_f32 v[60:61], v[60:61], v[6:7]
	v_cvt_f32_ubyte0_e32 v2, v214
	v_cvt_f32_ubyte1_e32 v3, v214
	v_cvt_f32_ubyte2_e32 v6, v214
	v_cvt_f32_ubyte3_e32 v7, v214
	v_rcp_iflag_f32_e32 v2, v2
	v_rcp_iflag_f32_e32 v3, v3
	v_rcp_iflag_f32_e32 v6, v6
	v_rcp_iflag_f32_e32 v7, v7
	v_cvt_f32_ubyte3_e32 v11, v202
	v_cvt_f32_ubyte2_e32 v10, v202
	v_cvt_f32_ubyte1_e32 v13, v202
	v_cvt_f32_ubyte0_e32 v12, v202
	v_pk_mul_f32 v[2:3], v[2:3], v[12:13]
	v_pk_mul_f32 v[6:7], v[6:7], v[10:11]
	v_cvt_f32_ubyte2_e32 v4, v215
	v_pk_mul_f32 v[56:57], v[56:57], v[6:7]
	v_pk_mul_f32 v[54:55], v[54:55], v[2:3]
	v_cvt_f32_ubyte0_e32 v2, v215
	v_cvt_f32_ubyte1_e32 v3, v215
	v_rcp_iflag_f32_e32 v6, v4
	v_cvt_f32_ubyte3_e32 v4, v215
	v_rcp_iflag_f32_e32 v2, v2
	v_rcp_iflag_f32_e32 v3, v3
	v_rcp_iflag_f32_e32 v7, v4
	v_cvt_f32_ubyte3_e32 v9, v203
	v_cvt_f32_ubyte2_e32 v8, v203
	v_cvt_f32_ubyte1_e32 v11, v203
	v_cvt_f32_ubyte0_e32 v10, v203
	v_pk_mul_f32 v[2:3], v[2:3], v[10:11]
	v_pk_mul_f32 v[4:5], v[6:7], v[8:9]
	v_pk_mul_f32 v[50:51], v[50:51], v[2:3]
	v_pk_mul_f32 v[52:53], v[52:53], v[4:5]
	s_waitcnt vmcnt(2)
	v_cvt_f32_ubyte1_e32 v17, v216
	v_cvt_f32_ubyte0_e32 v10, v240
	v_cvt_f32_ubyte1_e32 v11, v240
	v_rcp_iflag_f32_e32 v10, v10
	v_rcp_iflag_f32_e32 v11, v11
	v_cvt_f32_ubyte0_e32 v16, v216
	v_cvt_f32_ubyte3_e32 v15, v216
	v_cvt_f32_ubyte2_e32 v14, v216
	v_pk_mul_f32 v[10:11], v[10:11], v[16:17]
	v_cvt_f32_ubyte0_e32 v2, v241
	v_cvt_f32_ubyte2_e32 v12, v240
	v_cvt_f32_ubyte3_e32 v6, v240
	v_pk_mul_f32 v[46:47], v[46:47], v[10:11]
	v_rcp_iflag_f32_e32 v10, v2
	v_cvt_f32_ubyte1_e32 v2, v241
	v_rcp_iflag_f32_e32 v12, v12
	v_rcp_iflag_f32_e32 v13, v6
	v_rcp_iflag_f32_e32 v11, v2
	v_cvt_f32_ubyte2_e32 v2, v241
	v_rcp_iflag_f32_e32 v6, v2
	v_cvt_f32_ubyte3_e32 v2, v241
	v_rcp_iflag_f32_e32 v7, v2
	v_pk_mul_f32 v[12:13], v[12:13], v[14:15]
	v_cvt_f32_ubyte1_e32 v15, v217
	v_pk_mul_f32 v[48:49], v[48:49], v[12:13]
	v_cvt_f32_ubyte3_e32 v13, v217
	v_cvt_f32_ubyte2_e32 v12, v217
	v_cvt_f32_ubyte0_e32 v14, v217
	v_pk_mul_f32 v[2:3], v[10:11], v[14:15]
	v_pk_mul_f32 v[6:7], v[6:7], v[12:13]
	v_pk_mul_f32 v[42:43], v[42:43], v[2:3]
	v_pk_mul_f32 v[44:45], v[44:45], v[6:7]
	v_cvt_f32_ubyte0_e32 v2, v242
	v_cvt_f32_ubyte1_e32 v3, v242
	v_cvt_f32_ubyte2_e32 v6, v242
	v_cvt_f32_ubyte3_e32 v7, v242
	v_rcp_iflag_f32_e32 v2, v2
	v_rcp_iflag_f32_e32 v3, v3
	v_rcp_iflag_f32_e32 v6, v6
	v_rcp_iflag_f32_e32 v7, v7
	v_cvt_f32_ubyte3_e32 v11, v218
	v_cvt_f32_ubyte2_e32 v10, v218
	v_cvt_f32_ubyte1_e32 v13, v218
	v_cvt_f32_ubyte0_e32 v12, v218
	v_pk_mul_f32 v[2:3], v[2:3], v[12:13]
	v_pk_mul_f32 v[6:7], v[6:7], v[10:11]
	v_cvt_f32_ubyte2_e32 v4, v243
	v_pk_mul_f32 v[40:41], v[40:41], v[6:7]
	v_pk_mul_f32 v[38:39], v[38:39], v[2:3]
	v_cvt_f32_ubyte0_e32 v2, v243
	v_cvt_f32_ubyte1_e32 v3, v243
	v_rcp_iflag_f32_e32 v6, v4
	v_cvt_f32_ubyte3_e32 v4, v243
	v_rcp_iflag_f32_e32 v2, v2
	v_rcp_iflag_f32_e32 v3, v3
	v_rcp_iflag_f32_e32 v7, v4
	v_cvt_f32_ubyte3_e32 v9, v219
	v_cvt_f32_ubyte2_e32 v8, v219
	v_cvt_f32_ubyte1_e32 v11, v219
	v_cvt_f32_ubyte0_e32 v10, v219
	v_pk_mul_f32 v[2:3], v[2:3], v[10:11]
	v_pk_mul_f32 v[4:5], v[6:7], v[8:9]
	v_pk_mul_f32 v[34:35], v[34:35], v[2:3]
	v_pk_mul_f32 v[36:37], v[36:37], v[4:5]
	s_nop 0
	s_waitcnt vmcnt(0)
	v_cvt_f32_ubyte1_e32 v17, v152
	v_cvt_f32_ubyte0_e32 v0, v156
	v_rcp_iflag_f32_e32 v10, v0
	v_cvt_f32_ubyte1_e32 v0, v156
	v_rcp_iflag_f32_e32 v11, v0
	v_cvt_f32_ubyte2_e32 v0, v156
	v_rcp_iflag_f32_e32 v12, v0
	v_cvt_f32_ubyte3_e32 v0, v156
	v_cvt_f32_ubyte0_e32 v16, v152
	v_rcp_iflag_f32_e32 v13, v0
	v_pk_mul_f32 v[10:11], v[10:11], v[16:17]
	v_cvt_f32_ubyte0_e32 v0, v157
	v_pk_mul_f32 v[30:31], v[30:31], v[10:11]
	v_rcp_iflag_f32_e32 v10, v0
	v_cvt_f32_ubyte1_e32 v0, v157
	v_rcp_iflag_f32_e32 v11, v0
	v_cvt_f32_ubyte2_e32 v0, v157
	v_rcp_iflag_f32_e32 v6, v0
	v_cvt_f32_ubyte3_e32 v0, v157
	v_cvt_f32_ubyte3_e32 v15, v152
	v_cvt_f32_ubyte2_e32 v14, v152
	v_rcp_iflag_f32_e32 v7, v0
	v_pk_mul_f32 v[12:13], v[12:13], v[14:15]
	v_cvt_f32_ubyte1_e32 v15, v153
	v_cvt_f32_ubyte0_e32 v14, v153
	v_pk_mul_f32 v[32:33], v[32:33], v[12:13]
	v_cvt_f32_ubyte3_e32 v13, v153
	v_cvt_f32_ubyte2_e32 v12, v153
	v_pk_mul_f32 v[2:3], v[10:11], v[14:15]
	v_cvt_f32_ubyte0_e32 v0, v158
	v_pk_mul_f32 v[26:27], v[26:27], v[2:3]
	v_rcp_iflag_f32_e32 v2, v0
	v_cvt_f32_ubyte1_e32 v0, v158
	v_pk_mul_f32 v[6:7], v[6:7], v[12:13]
	v_rcp_iflag_f32_e32 v3, v0
	v_cvt_f32_ubyte2_e32 v0, v158
	v_pk_mul_f32 v[28:29], v[28:29], v[6:7]
	v_rcp_iflag_f32_e32 v6, v0
	v_cvt_f32_ubyte3_e32 v0, v158
	v_rcp_iflag_f32_e32 v7, v0
	v_cvt_f32_ubyte1_e32 v13, v154
	v_cvt_f32_ubyte0_e32 v12, v154
	v_pk_mul_f32 v[2:3], v[2:3], v[12:13]
	v_cvt_f32_ubyte0_e32 v0, v159
	v_cvt_f32_ubyte3_e32 v11, v154
	v_cvt_f32_ubyte2_e32 v10, v154
	v_pk_mul_f32 v[22:23], v[22:23], v[2:3]
	v_rcp_iflag_f32_e32 v2, v0
	v_cvt_f32_ubyte1_e32 v0, v159
	v_pk_mul_f32 v[6:7], v[6:7], v[10:11]
	v_rcp_iflag_f32_e32 v3, v0
	v_cvt_f32_ubyte2_e32 v0, v159
	v_pk_mul_f32 v[24:25], v[24:25], v[6:7]
	v_rcp_iflag_f32_e32 v6, v0
	v_cvt_f32_ubyte3_e32 v0, v159
	v_rcp_iflag_f32_e32 v7, v0
	v_cvt_f32_ubyte3_e32 v9, v155
	v_cvt_f32_ubyte2_e32 v8, v155
	v_cvt_f32_ubyte1_e32 v11, v155
	v_cvt_f32_ubyte0_e32 v10, v155
	v_pk_mul_f32 v[2:3], v[2:3], v[10:11]
	v_pk_mul_f32 v[4:5], v[6:7], v[8:9]
	v_pk_mul_f32 v[18:19], v[18:19], v[2:3]
	v_pk_mul_f32 v[20:21], v[20:21], v[4:5]
	s_nop 0
	s_nop 7

.LBB0_738:
	v_mov_b32_e32 v0, v165
	s_add_i32 s87, s87, s77
	s_nop 15
	s_nop 15
	s_movk_i32 s12, 0x1800
	v_and_or_b32 v2, v0, 15, s87
	v_mul_lo_u32 v3, v2, s12
	v_and_b32_e32 v0, -16, v0
	s_add_i32 s12, s82, s86
	v_add3_u32 v6, s12, v0, v3
	v_lshlrev_b32_e32 v2, 11, v2
	s_or_b32 s12, s86, s81
	v_add3_u32 v0, s12, v0, v2
	global_load_dwordx4 v[152:155], v6, s[46:47]
	v_add_u32_e32 v204, 0x18000, v6
	global_load_dwordx4 v[156:159], v204, s[46:47]
	v_add_u32_e32 v204, 0x30000, v6
	global_load_dwordx4 v[160:163], v204, s[46:47]
	v_add_u32_e32 v204, 0x48000, v6
	global_load_dwordx4 v[172:175], v204, s[46:47]
	v_add_u32_e32 v204, 0xc0000, v6
	global_load_dwordx4 v[176:179], v204, s[46:47]
	v_add_u32_e32 v204, 0xd8000, v6
	global_load_dwordx4 v[180:183], v204, s[46:47]
	v_add_u32_e32 v204, 0xf0000, v6
	global_load_dwordx4 v[184:187], v204, s[46:47]
	v_add_u32_e32 v204, 0x108000, v6
	global_load_dwordx4 v[188:191], v204, s[46:47]
	s_mov_b64 s[56:57], -1
	s_and_b64 vcc, exec, s[38:39]
	s_movk_i32 s89, 0xfe3f
	s_waitcnt vmcnt(7)
	v_cvt_f32_ubyte0_e32 v7, v152
	v_cvt_f32_ubyte1_e32 v8, v152
	v_mul_f32_e32 v7, 0x3b808081, v7
	v_mul_f32_e32 v8, 0x3b808081, v8
	v_cvt_f32_ubyte2_e32 v9, v152
	v_cvt_f32_ubyte3_e32 v2, v152
	v_mul_f32_e32 v7, v142, v7
	v_mul_f32_e32 v8, v143, v8
	v_mul_f32_e32 v2, 0x3b808081, v2
	v_mul_f32_e32 v10, v145, v2
	v_med3_f32 v7, v7, s19, v229
	v_med3_f32 v8, v8, s19, v229
	v_mov_b32_e32 v2, v1
	v_cvt_pk_fp8_f32 v2, v7, v8
	v_mul_f32_e32 v9, 0x3b808081, v9
	v_mul_f32_e32 v9, v144, v9
	v_med3_f32 v7, v9, s19, v229
	v_med3_f32 v8, v10, s19, v229
	v_cvt_pk_fp8_f32 v2, v7, v8 op_sel:[0,0,1]
	v_cvt_f32_ubyte0_e32 v7, v153
	v_cvt_f32_ubyte1_e32 v8, v153
	v_mul_f32_e32 v7, 0x3b808081, v7
	v_mul_f32_e32 v8, 0x3b808081, v8
	v_cvt_f32_ubyte2_e32 v9, v153
	v_cvt_f32_ubyte3_e32 v3, v153
	v_mul_f32_e32 v7, v138, v7
	v_mul_f32_e32 v8, v139, v8
	v_mul_f32_e32 v3, 0x3b808081, v3
	v_mul_f32_e32 v10, v141, v3
	v_med3_f32 v7, v7, s19, v229
	v_med3_f32 v8, v8, s19, v229
	v_mov_b32_e32 v3, v1
	v_cvt_pk_fp8_f32 v3, v7, v8
	v_mul_f32_e32 v9, 0x3b808081, v9
	v_mul_f32_e32 v9, v140, v9
	v_med3_f32 v7, v9, s19, v229
	v_med3_f32 v8, v10, s19, v229
	v_cvt_pk_fp8_f32 v3, v7, v8 op_sel:[0,0,1]
	v_cvt_f32_ubyte0_e32 v7, v154
	v_cvt_f32_ubyte1_e32 v8, v154
	v_mul_f32_e32 v7, 0x3b808081, v7
	v_mul_f32_e32 v8, 0x3b808081, v8
	v_cvt_f32_ubyte2_e32 v9, v154
	v_cvt_f32_ubyte3_e32 v4, v154
	v_mul_f32_e32 v7, v134, v7
	v_mul_f32_e32 v8, v135, v8
	v_mul_f32_e32 v4, 0x3b808081, v4
	v_mul_f32_e32 v10, v137, v4
	v_med3_f32 v7, v7, s19, v229
	v_med3_f32 v8, v8, s19, v229
	v_mov_b32_e32 v4, v1
	v_cvt_pk_fp8_f32 v4, v7, v8
	v_mul_f32_e32 v9, 0x3b808081, v9
	v_mul_f32_e32 v9, v136, v9
	v_med3_f32 v7, v9, s19, v229
	v_med3_f32 v8, v10, s19, v229
	v_cvt_pk_fp8_f32 v4, v7, v8 op_sel:[0,0,1]
	v_cvt_f32_ubyte0_e32 v7, v155
	v_cvt_f32_ubyte1_e32 v8, v155
	v_mul_f32_e32 v7, 0x3b808081, v7
	v_mul_f32_e32 v8, 0x3b808081, v8
	v_cvt_f32_ubyte2_e32 v9, v155
	v_cvt_f32_ubyte3_e32 v5, v155
	v_mul_f32_e32 v7, v130, v7
	v_mul_f32_e32 v8, v131, v8
	v_mul_f32_e32 v5, 0x3b808081, v5
	v_mul_f32_e32 v10, v133, v5
	v_med3_f32 v7, v7, s19, v229
	v_med3_f32 v8, v8, s19, v229
	v_mov_b32_e32 v5, v1
	v_cvt_pk_fp8_f32 v5, v7, v8
	v_mul_f32_e32 v9, 0x3b808081, v9
	v_mul_f32_e32 v9, v132, v9
	v_med3_f32 v7, v9, s19, v229
	v_med3_f32 v8, v10, s19, v229
	v_cvt_pk_fp8_f32 v5, v7, v8 op_sel:[0,0,1]
	global_store_dwordx4 v0, v[2:5], s[48:49]
	s_nop 1
	s_waitcnt vmcnt(7)
	v_cvt_f32_ubyte0_e32 v7, v156
	v_cvt_f32_ubyte1_e32 v8, v156
	v_mul_f32_e32 v7, 0x3b808081, v7
	v_mul_f32_e32 v8, 0x3b808081, v8
	v_cvt_f32_ubyte2_e32 v9, v156
	v_cvt_f32_ubyte3_e32 v2, v156
	v_mul_f32_e32 v7, v126, v7
	v_mul_f32_e32 v8, v127, v8
	v_mul_f32_e32 v2, 0x3b808081, v2
	v_mul_f32_e32 v10, v129, v2
	v_med3_f32 v7, v7, s19, v229
	v_med3_f32 v8, v8, s19, v229
	v_mov_b32_e32 v2, v1
	v_cvt_pk_fp8_f32 v2, v7, v8
	v_mul_f32_e32 v9, 0x3b808081, v9
	v_mul_f32_e32 v9, v128, v9
	v_med3_f32 v7, v9, s19, v229
	v_med3_f32 v8, v10, s19, v229
	v_cvt_pk_fp8_f32 v2, v7, v8 op_sel:[0,0,1]
	v_cvt_f32_ubyte0_e32 v7, v157
	v_cvt_f32_ubyte1_e32 v8, v157
	v_mul_f32_e32 v7, 0x3b808081, v7
	v_mul_f32_e32 v8, 0x3b808081, v8
	v_cvt_f32_ubyte2_e32 v9, v157
	v_cvt_f32_ubyte3_e32 v3, v157
	v_mul_f32_e32 v7, v122, v7
	v_mul_f32_e32 v8, v123, v8
	v_mul_f32_e32 v3, 0x3b808081, v3
	v_mul_f32_e32 v10, v125, v3
	v_med3_f32 v7, v7, s19, v229
	v_med3_f32 v8, v8, s19, v229
	v_mov_b32_e32 v3, v1
	v_cvt_pk_fp8_f32 v3, v7, v8
	v_mul_f32_e32 v9, 0x3b808081, v9
	v_mul_f32_e32 v9, v124, v9
	v_med3_f32 v7, v9, s19, v229
	v_med3_f32 v8, v10, s19, v229
	v_cvt_pk_fp8_f32 v3, v7, v8 op_sel:[0,0,1]
	v_cvt_f32_ubyte0_e32 v7, v158
	v_cvt_f32_ubyte1_e32 v8, v158
	v_mul_f32_e32 v7, 0x3b808081, v7
	v_mul_f32_e32 v8, 0x3b808081, v8
	v_cvt_f32_ubyte2_e32 v9, v158
	v_cvt_f32_ubyte3_e32 v4, v158
	v_mul_f32_e32 v7, v118, v7
	v_mul_f32_e32 v8, v119, v8
	v_mul_f32_e32 v4, 0x3b808081, v4
	v_mul_f32_e32 v10, v121, v4
	v_med3_f32 v7, v7, s19, v229
	v_med3_f32 v8, v8, s19, v229
	v_mov_b32_e32 v4, v1
	v_cvt_pk_fp8_f32 v4, v7, v8
	v_mul_f32_e32 v9, 0x3b808081, v9
	v_mul_f32_e32 v9, v120, v9
	v_med3_f32 v7, v9, s19, v229
	v_med3_f32 v8, v10, s19, v229
	v_cvt_pk_fp8_f32 v4, v7, v8 op_sel:[0,0,1]
	v_cvt_f32_ubyte0_e32 v7, v159
	v_cvt_f32_ubyte1_e32 v8, v159
	v_mul_f32_e32 v7, 0x3b808081, v7
	v_mul_f32_e32 v8, 0x3b808081, v8
	v_cvt_f32_ubyte2_e32 v9, v159
	v_cvt_f32_ubyte3_e32 v5, v159
	v_mul_f32_e32 v7, v114, v7
	v_mul_f32_e32 v8, v115, v8
	v_mul_f32_e32 v5, 0x3b808081, v5
	v_mul_f32_e32 v10, v117, v5
	v_med3_f32 v7, v7, s19, v229
	v_med3_f32 v8, v8, s19, v229
	v_mov_b32_e32 v5, v1
	v_cvt_pk_fp8_f32 v5, v7, v8
	v_mul_f32_e32 v9, 0x3b808081, v9
	v_mul_f32_e32 v9, v116, v9
	v_med3_f32 v7, v9, s19, v229
	v_med3_f32 v8, v10, s19, v229
	v_cvt_pk_fp8_f32 v5, v7, v8 op_sel:[0,0,1]
	v_add_u32_e32 v7, 0x8000, v0
	global_store_dwordx4 v7, v[2:5], s[48:49]
	s_nop 1
	s_waitcnt vmcnt(7)
	v_cvt_f32_ubyte0_e32 v7, v160
	v_cvt_f32_ubyte1_e32 v8, v160
	v_mul_f32_e32 v7, 0x3b808081, v7
	v_mul_f32_e32 v8, 0x3b808081, v8
	v_cvt_f32_ubyte2_e32 v9, v160
	v_cvt_f32_ubyte3_e32 v2, v160
	v_mul_f32_e32 v7, v110, v7
	v_mul_f32_e32 v8, v111, v8
	v_mul_f32_e32 v2, 0x3b808081, v2
	v_mul_f32_e32 v10, v113, v2
	v_med3_f32 v7, v7, s19, v229
	v_med3_f32 v8, v8, s19, v229
	v_mov_b32_e32 v2, v1
	v_cvt_pk_fp8_f32 v2, v7, v8
	v_mul_f32_e32 v9, 0x3b808081, v9
	v_mul_f32_e32 v9, v112, v9
	v_med3_f32 v7, v9, s19, v229
	v_med3_f32 v8, v10, s19, v229
	v_cvt_pk_fp8_f32 v2, v7, v8 op_sel:[0,0,1]
	v_cvt_f32_ubyte0_e32 v7, v161
	v_cvt_f32_ubyte1_e32 v8, v161
	v_mul_f32_e32 v7, 0x3b808081, v7
	v_mul_f32_e32 v8, 0x3b808081, v8
	v_cvt_f32_ubyte2_e32 v9, v161
	v_cvt_f32_ubyte3_e32 v3, v161
	v_mul_f32_e32 v7, v106, v7
	v_mul_f32_e32 v8, v107, v8
	v_mul_f32_e32 v3, 0x3b808081, v3
	v_mul_f32_e32 v10, v109, v3
	v_med3_f32 v7, v7, s19, v229
	v_med3_f32 v8, v8, s19, v229
	v_mov_b32_e32 v3, v1
	v_cvt_pk_fp8_f32 v3, v7, v8
	v_mul_f32_e32 v9, 0x3b808081, v9
	v_mul_f32_e32 v9, v108, v9
	v_med3_f32 v7, v9, s19, v229
	v_med3_f32 v8, v10, s19, v229
	v_cvt_pk_fp8_f32 v3, v7, v8 op_sel:[0,0,1]
	v_cvt_f32_ubyte0_e32 v7, v162
	v_cvt_f32_ubyte1_e32 v8, v162
	v_mul_f32_e32 v7, 0x3b808081, v7
	v_mul_f32_e32 v8, 0x3b808081, v8
	v_cvt_f32_ubyte2_e32 v9, v162
	v_cvt_f32_ubyte3_e32 v4, v162
	v_mul_f32_e32 v7, v102, v7
	v_mul_f32_e32 v8, v103, v8
	v_mul_f32_e32 v4, 0x3b808081, v4
	v_mul_f32_e32 v10, v105, v4
	v_med3_f32 v7, v7, s19, v229
	v_med3_f32 v8, v8, s19, v229
	v_mov_b32_e32 v4, v1
	v_cvt_pk_fp8_f32 v4, v7, v8
	v_mul_f32_e32 v9, 0x3b808081, v9
	v_mul_f32_e32 v9, v104, v9
	v_med3_f32 v7, v9, s19, v229
	v_med3_f32 v8, v10, s19, v229
	v_cvt_pk_fp8_f32 v4, v7, v8 op_sel:[0,0,1]
	v_cvt_f32_ubyte0_e32 v7, v163
	v_cvt_f32_ubyte1_e32 v8, v163
	v_mul_f32_e32 v7, 0x3b808081, v7
	v_mul_f32_e32 v8, 0x3b808081, v8
	v_cvt_f32_ubyte2_e32 v9, v163
	v_cvt_f32_ubyte3_e32 v5, v163
	v_mul_f32_e32 v7, v98, v7
	v_mul_f32_e32 v8, v99, v8
	v_mul_f32_e32 v5, 0x3b808081, v5
	v_mul_f32_e32 v10, v101, v5
	v_med3_f32 v7, v7, s19, v229
	v_med3_f32 v8, v8, s19, v229
	v_mov_b32_e32 v5, v1
	v_cvt_pk_fp8_f32 v5, v7, v8
	v_mul_f32_e32 v9, 0x3b808081, v9
	v_mul_f32_e32 v9, v100, v9
	v_med3_f32 v7, v9, s19, v229
	v_med3_f32 v8, v10, s19, v229
	v_cvt_pk_fp8_f32 v5, v7, v8 op_sel:[0,0,1]
	v_add_u32_e32 v7, 0x10000, v0
	global_store_dwordx4 v7, v[2:5], s[48:49]
	s_nop 1
	s_waitcnt vmcnt(7)
	v_cvt_f32_ubyte0_e32 v7, v172
	v_cvt_f32_ubyte1_e32 v8, v172
	v_mul_f32_e32 v7, 0x3b808081, v7
	v_mul_f32_e32 v8, 0x3b808081, v8
	v_cvt_f32_ubyte2_e32 v9, v172
	v_cvt_f32_ubyte3_e32 v2, v172
	v_mul_f32_e32 v7, v94, v7
	v_mul_f32_e32 v8, v95, v8
	v_mul_f32_e32 v2, 0x3b808081, v2
	v_mul_f32_e32 v10, v97, v2
	v_med3_f32 v7, v7, s19, v229
	v_med3_f32 v8, v8, s19, v229
	v_mov_b32_e32 v2, v1
	v_cvt_pk_fp8_f32 v2, v7, v8
	v_mul_f32_e32 v9, 0x3b808081, v9
	v_mul_f32_e32 v9, v96, v9
	v_med3_f32 v7, v9, s19, v229
	v_med3_f32 v8, v10, s19, v229
	v_cvt_pk_fp8_f32 v2, v7, v8 op_sel:[0,0,1]
	v_cvt_f32_ubyte0_e32 v7, v173
	v_cvt_f32_ubyte1_e32 v8, v173
	v_mul_f32_e32 v7, 0x3b808081, v7
	v_mul_f32_e32 v8, 0x3b808081, v8
	v_cvt_f32_ubyte2_e32 v9, v173
	v_cvt_f32_ubyte3_e32 v3, v173
	v_mul_f32_e32 v7, v90, v7
	v_mul_f32_e32 v8, v91, v8
	v_mul_f32_e32 v3, 0x3b808081, v3
	v_mul_f32_e32 v10, v93, v3
	v_med3_f32 v7, v7, s19, v229
	v_med3_f32 v8, v8, s19, v229
	v_mov_b32_e32 v3, v1
	v_cvt_pk_fp8_f32 v3, v7, v8
	v_mul_f32_e32 v9, 0x3b808081, v9
	v_mul_f32_e32 v9, v92, v9
	v_med3_f32 v7, v9, s19, v229
	v_med3_f32 v8, v10, s19, v229
	v_cvt_pk_fp8_f32 v3, v7, v8 op_sel:[0,0,1]
	v_cvt_f32_ubyte0_e32 v7, v174
	v_cvt_f32_ubyte1_e32 v8, v174
	v_mul_f32_e32 v7, 0x3b808081, v7
	v_mul_f32_e32 v8, 0x3b808081, v8
	v_cvt_f32_ubyte2_e32 v9, v174
	v_cvt_f32_ubyte3_e32 v4, v174
	v_mul_f32_e32 v7, v86, v7
	v_mul_f32_e32 v8, v87, v8
	v_mul_f32_e32 v4, 0x3b808081, v4
	v_mul_f32_e32 v10, v89, v4
	v_med3_f32 v7, v7, s19, v229
	v_med3_f32 v8, v8, s19, v229
	v_mov_b32_e32 v4, v1
	v_cvt_pk_fp8_f32 v4, v7, v8
	v_mul_f32_e32 v9, 0x3b808081, v9
	v_mul_f32_e32 v9, v88, v9
	v_med3_f32 v7, v9, s19, v229
	v_med3_f32 v8, v10, s19, v229
	v_cvt_pk_fp8_f32 v4, v7, v8 op_sel:[0,0,1]
	v_cvt_f32_ubyte0_e32 v7, v175
	v_cvt_f32_ubyte1_e32 v8, v175
	v_mul_f32_e32 v7, 0x3b808081, v7
	v_mul_f32_e32 v8, 0x3b808081, v8
	v_cvt_f32_ubyte2_e32 v9, v175
	v_cvt_f32_ubyte3_e32 v5, v175
	v_mul_f32_e32 v7, v82, v7
	v_mul_f32_e32 v8, v83, v8
	v_mul_f32_e32 v5, 0x3b808081, v5
	v_mul_f32_e32 v10, v85, v5
	v_med3_f32 v7, v7, s19, v229
	v_med3_f32 v8, v8, s19, v229
	v_mov_b32_e32 v5, v1
	v_cvt_pk_fp8_f32 v5, v7, v8
	v_mul_f32_e32 v9, 0x3b808081, v9
	v_mul_f32_e32 v9, v84, v9
	v_med3_f32 v7, v9, s19, v229
	v_med3_f32 v8, v10, s19, v229
	v_cvt_pk_fp8_f32 v5, v7, v8 op_sel:[0,0,1]
	v_add_u32_e32 v7, 0x18000, v0
	global_store_dwordx4 v7, v[2:5], s[48:49]
	s_nop 1
	s_waitcnt vmcnt(7)
	v_cvt_f32_ubyte0_e32 v7, v176
	v_cvt_f32_ubyte1_e32 v8, v176
	v_mul_f32_e32 v7, 0x3b808081, v7
	v_mul_f32_e32 v8, 0x3b808081, v8
	v_cvt_f32_ubyte2_e32 v9, v176
	v_cvt_f32_ubyte3_e32 v2, v176
	v_mul_f32_e32 v7, v78, v7
	v_mul_f32_e32 v8, v79, v8
	v_mul_f32_e32 v2, 0x3b808081, v2
	v_mul_f32_e32 v10, v81, v2
	v_med3_f32 v7, v7, s19, v229
	v_med3_f32 v8, v8, s19, v229
	v_mov_b32_e32 v2, v1
	v_cvt_pk_fp8_f32 v2, v7, v8
	v_mul_f32_e32 v9, 0x3b808081, v9
	v_mul_f32_e32 v9, v80, v9
	v_med3_f32 v7, v9, s19, v229
	v_med3_f32 v8, v10, s19, v229
	v_cvt_pk_fp8_f32 v2, v7, v8 op_sel:[0,0,1]
	v_cvt_f32_ubyte0_e32 v7, v177
	v_cvt_f32_ubyte1_e32 v8, v177
	v_mul_f32_e32 v7, 0x3b808081, v7
	v_mul_f32_e32 v8, 0x3b808081, v8
	v_cvt_f32_ubyte2_e32 v9, v177
	v_cvt_f32_ubyte3_e32 v3, v177
	v_mul_f32_e32 v7, v74, v7
	v_mul_f32_e32 v8, v75, v8
	v_mul_f32_e32 v3, 0x3b808081, v3
	v_mul_f32_e32 v10, v77, v3
	v_med3_f32 v7, v7, s19, v229
	v_med3_f32 v8, v8, s19, v229
	v_mov_b32_e32 v3, v1
	v_cvt_pk_fp8_f32 v3, v7, v8
	v_mul_f32_e32 v9, 0x3b808081, v9
	v_mul_f32_e32 v9, v76, v9
	v_med3_f32 v7, v9, s19, v229
	v_med3_f32 v8, v10, s19, v229
	v_cvt_pk_fp8_f32 v3, v7, v8 op_sel:[0,0,1]
	v_cvt_f32_ubyte0_e32 v7, v178
	v_cvt_f32_ubyte1_e32 v8, v178
	v_mul_f32_e32 v7, 0x3b808081, v7
	v_mul_f32_e32 v8, 0x3b808081, v8
	v_cvt_f32_ubyte2_e32 v9, v178
	v_cvt_f32_ubyte3_e32 v4, v178
	v_mul_f32_e32 v7, v70, v7
	v_mul_f32_e32 v8, v71, v8
	v_mul_f32_e32 v4, 0x3b808081, v4
	v_mul_f32_e32 v10, v73, v4
	v_med3_f32 v7, v7, s19, v229
	v_med3_f32 v8, v8, s19, v229
	v_mov_b32_e32 v4, v1
	v_cvt_pk_fp8_f32 v4, v7, v8
	v_mul_f32_e32 v9, 0x3b808081, v9
	v_mul_f32_e32 v9, v72, v9
	v_med3_f32 v7, v9, s19, v229
	v_med3_f32 v8, v10, s19, v229
	v_cvt_pk_fp8_f32 v4, v7, v8 op_sel:[0,0,1]
	v_cvt_f32_ubyte0_e32 v7, v179
	v_cvt_f32_ubyte1_e32 v8, v179
	v_mul_f32_e32 v7, 0x3b808081, v7
	v_mul_f32_e32 v8, 0x3b808081, v8
	v_cvt_f32_ubyte2_e32 v9, v179
	v_cvt_f32_ubyte3_e32 v5, v179
	v_mul_f32_e32 v7, v66, v7
	v_mul_f32_e32 v8, v67, v8
	v_mul_f32_e32 v5, 0x3b808081, v5
	v_mul_f32_e32 v10, v69, v5
	v_med3_f32 v7, v7, s19, v229
	v_med3_f32 v8, v8, s19, v229
	v_mov_b32_e32 v5, v1
	v_cvt_pk_fp8_f32 v5, v7, v8
	v_mul_f32_e32 v9, 0x3b808081, v9
	v_mul_f32_e32 v9, v68, v9
	v_med3_f32 v7, v9, s19, v229
	v_med3_f32 v8, v10, s19, v229
	v_cvt_pk_fp8_f32 v5, v7, v8 op_sel:[0,0,1]
	v_add_u32_e32 v7, 0x40000, v0
	global_store_dwordx4 v7, v[2:5], s[48:49]
	s_nop 1
	s_waitcnt vmcnt(7)
	v_cvt_f32_ubyte0_e32 v7, v180
	v_cvt_f32_ubyte1_e32 v8, v180
	v_mul_f32_e32 v7, 0x3b808081, v7
	v_mul_f32_e32 v8, 0x3b808081, v8
	v_cvt_f32_ubyte2_e32 v9, v180
	v_cvt_f32_ubyte3_e32 v2, v180
	v_mul_f32_e32 v7, v62, v7
	v_mul_f32_e32 v8, v63, v8
	v_mul_f32_e32 v2, 0x3b808081, v2
	v_mul_f32_e32 v10, v65, v2
	v_med3_f32 v7, v7, s19, v229
	v_med3_f32 v8, v8, s19, v229
	v_mov_b32_e32 v2, v1
	v_cvt_pk_fp8_f32 v2, v7, v8
	v_mul_f32_e32 v9, 0x3b808081, v9
	v_mul_f32_e32 v9, v64, v9
	v_med3_f32 v7, v9, s19, v229
	v_med3_f32 v8, v10, s19, v229
	v_cvt_pk_fp8_f32 v2, v7, v8 op_sel:[0,0,1]
	v_cvt_f32_ubyte0_e32 v7, v181
	v_cvt_f32_ubyte1_e32 v8, v181
	v_mul_f32_e32 v7, 0x3b808081, v7
	v_mul_f32_e32 v8, 0x3b808081, v8
	v_cvt_f32_ubyte2_e32 v9, v181
	v_cvt_f32_ubyte3_e32 v3, v181
	v_mul_f32_e32 v7, v58, v7
	v_mul_f32_e32 v8, v59, v8
	v_mul_f32_e32 v3, 0x3b808081, v3
	v_mul_f32_e32 v10, v61, v3
	v_med3_f32 v7, v7, s19, v229
	v_med3_f32 v8, v8, s19, v229
	v_mov_b32_e32 v3, v1
	v_cvt_pk_fp8_f32 v3, v7, v8
	v_mul_f32_e32 v9, 0x3b808081, v9
	v_mul_f32_e32 v9, v60, v9
	v_med3_f32 v7, v9, s19, v229
	v_med3_f32 v8, v10, s19, v229
	v_cvt_pk_fp8_f32 v3, v7, v8 op_sel:[0,0,1]
	v_cvt_f32_ubyte0_e32 v7, v182
	v_cvt_f32_ubyte1_e32 v8, v182
	v_mul_f32_e32 v7, 0x3b808081, v7
	v_mul_f32_e32 v8, 0x3b808081, v8
	v_cvt_f32_ubyte2_e32 v9, v182
	v_cvt_f32_ubyte3_e32 v4, v182
	v_mul_f32_e32 v7, v54, v7
	v_mul_f32_e32 v8, v55, v8
	v_mul_f32_e32 v4, 0x3b808081, v4
	v_mul_f32_e32 v10, v57, v4
	v_med3_f32 v7, v7, s19, v229
	v_med3_f32 v8, v8, s19, v229
	v_mov_b32_e32 v4, v1
	v_cvt_pk_fp8_f32 v4, v7, v8
	v_mul_f32_e32 v9, 0x3b808081, v9
	v_mul_f32_e32 v9, v56, v9
	v_med3_f32 v7, v9, s19, v229
	v_med3_f32 v8, v10, s19, v229
	v_cvt_pk_fp8_f32 v4, v7, v8 op_sel:[0,0,1]
	v_cvt_f32_ubyte0_e32 v7, v183
	v_cvt_f32_ubyte1_e32 v8, v183
	v_mul_f32_e32 v7, 0x3b808081, v7
	v_mul_f32_e32 v8, 0x3b808081, v8
	v_cvt_f32_ubyte2_e32 v9, v183
	v_cvt_f32_ubyte3_e32 v5, v183
	v_mul_f32_e32 v7, v50, v7
	v_mul_f32_e32 v8, v51, v8
	v_mul_f32_e32 v5, 0x3b808081, v5
	v_mul_f32_e32 v10, v53, v5
	v_med3_f32 v7, v7, s19, v229
	v_med3_f32 v8, v8, s19, v229
	v_mov_b32_e32 v5, v1
	v_cvt_pk_fp8_f32 v5, v7, v8
	v_mul_f32_e32 v9, 0x3b808081, v9
	v_mul_f32_e32 v9, v52, v9
	v_med3_f32 v7, v9, s19, v229
	v_med3_f32 v8, v10, s19, v229
	v_cvt_pk_fp8_f32 v5, v7, v8 op_sel:[0,0,1]
	v_add_u32_e32 v7, 0x48000, v0
	global_store_dwordx4 v7, v[2:5], s[48:49]
	s_nop 1
	s_waitcnt vmcnt(7)
	v_cvt_f32_ubyte0_e32 v7, v184
	v_cvt_f32_ubyte1_e32 v8, v184
	v_mul_f32_e32 v7, 0x3b808081, v7
	v_mul_f32_e32 v8, 0x3b808081, v8
	v_cvt_f32_ubyte2_e32 v9, v184
	v_cvt_f32_ubyte3_e32 v2, v184
	v_mul_f32_e32 v7, v46, v7
	v_mul_f32_e32 v8, v47, v8
	v_mul_f32_e32 v2, 0x3b808081, v2
	v_mul_f32_e32 v10, v49, v2
	v_med3_f32 v7, v7, s19, v229
	v_med3_f32 v8, v8, s19, v229
	v_mov_b32_e32 v2, v1
	v_cvt_pk_fp8_f32 v2, v7, v8
	v_mul_f32_e32 v9, 0x3b808081, v9
	v_mul_f32_e32 v9, v48, v9
	v_med3_f32 v7, v9, s19, v229
	v_med3_f32 v8, v10, s19, v229
	v_cvt_pk_fp8_f32 v2, v7, v8 op_sel:[0,0,1]
	v_cvt_f32_ubyte0_e32 v7, v185
	v_cvt_f32_ubyte1_e32 v8, v185
	v_mul_f32_e32 v7, 0x3b808081, v7
	v_mul_f32_e32 v8, 0x3b808081, v8
	v_cvt_f32_ubyte2_e32 v9, v185
	v_cvt_f32_ubyte3_e32 v3, v185
	v_mul_f32_e32 v7, v42, v7
	v_mul_f32_e32 v8, v43, v8
	v_mul_f32_e32 v3, 0x3b808081, v3
	v_mul_f32_e32 v10, v45, v3
	v_med3_f32 v7, v7, s19, v229
	v_med3_f32 v8, v8, s19, v229
	v_mov_b32_e32 v3, v1
	v_cvt_pk_fp8_f32 v3, v7, v8
	v_mul_f32_e32 v9, 0x3b808081, v9
	v_mul_f32_e32 v9, v44, v9
	v_med3_f32 v7, v9, s19, v229
	v_med3_f32 v8, v10, s19, v229
	v_cvt_pk_fp8_f32 v3, v7, v8 op_sel:[0,0,1]
	v_cvt_f32_ubyte0_e32 v7, v186
	v_cvt_f32_ubyte1_e32 v8, v186
	v_mul_f32_e32 v7, 0x3b808081, v7
	v_mul_f32_e32 v8, 0x3b808081, v8
	v_cvt_f32_ubyte2_e32 v9, v186
	v_cvt_f32_ubyte3_e32 v4, v186
	v_mul_f32_e32 v7, v38, v7
	v_mul_f32_e32 v8, v39, v8
	v_mul_f32_e32 v4, 0x3b808081, v4
	v_mul_f32_e32 v10, v41, v4
	v_med3_f32 v7, v7, s19, v229
	v_med3_f32 v8, v8, s19, v229
	v_mov_b32_e32 v4, v1
	v_cvt_pk_fp8_f32 v4, v7, v8
	v_mul_f32_e32 v9, 0x3b808081, v9
	v_mul_f32_e32 v9, v40, v9
	v_med3_f32 v7, v9, s19, v229
	v_med3_f32 v8, v10, s19, v229
	v_cvt_pk_fp8_f32 v4, v7, v8 op_sel:[0,0,1]
	v_cvt_f32_ubyte0_e32 v7, v187
	v_cvt_f32_ubyte1_e32 v8, v187
	v_mul_f32_e32 v7, 0x3b808081, v7
	v_mul_f32_e32 v8, 0x3b808081, v8
	v_cvt_f32_ubyte2_e32 v9, v187
	v_cvt_f32_ubyte3_e32 v5, v187
	v_mul_f32_e32 v7, v34, v7
	v_mul_f32_e32 v8, v35, v8
	v_mul_f32_e32 v5, 0x3b808081, v5
	v_mul_f32_e32 v10, v37, v5
	v_med3_f32 v7, v7, s19, v229
	v_med3_f32 v8, v8, s19, v229
	v_mov_b32_e32 v5, v1
	v_cvt_pk_fp8_f32 v5, v7, v8
	v_mul_f32_e32 v9, 0x3b808081, v9
	v_mul_f32_e32 v9, v36, v9
	v_med3_f32 v7, v9, s19, v229
	v_med3_f32 v8, v10, s19, v229
	v_cvt_pk_fp8_f32 v5, v7, v8 op_sel:[0,0,1]
	v_add_u32_e32 v7, 0x50000, v0
	v_add_u32_e32 v0, 0x58000, v0
	global_store_dwordx4 v7, v[2:5], s[48:49]
	s_nop 1
	s_waitcnt vmcnt(7)
	v_cvt_f32_ubyte0_e32 v6, v188
	v_cvt_f32_ubyte1_e32 v7, v188
	v_mul_f32_e32 v6, 0x3b808081, v6
	v_mul_f32_e32 v7, 0x3b808081, v7
	v_cvt_f32_ubyte2_e32 v8, v188
	v_cvt_f32_ubyte3_e32 v2, v188
	v_mul_f32_e32 v6, v30, v6
	v_mul_f32_e32 v7, v31, v7
	v_mul_f32_e32 v2, 0x3b808081, v2
	v_mul_f32_e32 v9, v33, v2
	v_med3_f32 v6, v6, s19, v229
	v_med3_f32 v7, v7, s19, v229
	v_mov_b32_e32 v2, v1
	v_cvt_pk_fp8_f32 v2, v6, v7
	v_mul_f32_e32 v8, 0x3b808081, v8
	v_mul_f32_e32 v8, v32, v8
	v_med3_f32 v6, v8, s19, v229
	v_med3_f32 v7, v9, s19, v229
	v_cvt_pk_fp8_f32 v2, v6, v7 op_sel:[0,0,1]
	v_cvt_f32_ubyte0_e32 v6, v189
	v_cvt_f32_ubyte1_e32 v7, v189
	v_mul_f32_e32 v6, 0x3b808081, v6
	v_mul_f32_e32 v7, 0x3b808081, v7
	v_cvt_f32_ubyte2_e32 v8, v189
	v_cvt_f32_ubyte3_e32 v3, v189
	v_mul_f32_e32 v6, v26, v6
	v_mul_f32_e32 v7, v27, v7
	v_mul_f32_e32 v3, 0x3b808081, v3
	v_mul_f32_e32 v9, v29, v3
	v_med3_f32 v6, v6, s19, v229
	v_med3_f32 v7, v7, s19, v229
	v_mov_b32_e32 v3, v1
	v_cvt_pk_fp8_f32 v3, v6, v7
	v_mul_f32_e32 v8, 0x3b808081, v8
	v_mul_f32_e32 v8, v28, v8
	v_med3_f32 v6, v8, s19, v229
	v_med3_f32 v7, v9, s19, v229
	v_cvt_pk_fp8_f32 v3, v6, v7 op_sel:[0,0,1]
	v_cvt_f32_ubyte0_e32 v6, v190
	v_cvt_f32_ubyte1_e32 v7, v190
	v_mul_f32_e32 v6, 0x3b808081, v6
	v_mul_f32_e32 v7, 0x3b808081, v7
	v_cvt_f32_ubyte2_e32 v8, v190
	v_cvt_f32_ubyte3_e32 v4, v190
	v_mul_f32_e32 v6, v22, v6
	v_mul_f32_e32 v7, v23, v7
	v_mul_f32_e32 v4, 0x3b808081, v4
	v_mul_f32_e32 v9, v25, v4
	v_med3_f32 v6, v6, s19, v229
	v_med3_f32 v7, v7, s19, v229
	v_mov_b32_e32 v4, v1
	v_cvt_pk_fp8_f32 v4, v6, v7
	v_mul_f32_e32 v8, 0x3b808081, v8
	v_mul_f32_e32 v8, v24, v8
	v_med3_f32 v6, v8, s19, v229
	v_med3_f32 v7, v9, s19, v229
	v_cvt_pk_fp8_f32 v4, v6, v7 op_sel:[0,0,1]
	v_cvt_f32_ubyte0_e32 v6, v191
	v_cvt_f32_ubyte1_e32 v7, v191
	v_mul_f32_e32 v6, 0x3b808081, v6
	v_mul_f32_e32 v7, 0x3b808081, v7
	v_cvt_f32_ubyte2_e32 v8, v191
	v_cvt_f32_ubyte3_e32 v5, v191
	v_mul_f32_e32 v6, v18, v6
	v_mul_f32_e32 v7, v19, v7
	v_mul_f32_e32 v5, 0x3b808081, v5
	v_mul_f32_e32 v9, v21, v5
	v_med3_f32 v6, v6, s19, v229
	v_med3_f32 v7, v7, s19, v229
	v_mov_b32_e32 v5, v1
	v_cvt_pk_fp8_f32 v5, v6, v7
	v_mul_f32_e32 v8, 0x3b808081, v8
	v_mul_f32_e32 v8, v20, v8
	v_med3_f32 v6, v8, s19, v229
	v_med3_f32 v7, v9, s19, v229
	v_cvt_pk_fp8_f32 v5, v6, v7 op_sel:[0,0,1]
	global_store_dwordx4 v0, v[2:5], s[48:49]
	s_cbranch_vccnz .LBB0_718
	s_andn2_b64 vcc, exec, s[44:45]
	s_cbranch_vccnz .LBB0_717
	s_barrier
	s_branch .LBB0_717

.LBB0_820:
	v_mov_b32_e32 v0, v183
	s_lshl_b32 s12, s12, 8
	s_nop 15
	s_nop 15
	s_add_i32 s12, s12, s68
	v_and_or_b32 v2, v0, 15, s12
	s_lshl_b32 s12, s18, 8
	v_ashrrev_i32_e32 v0, 1, v0
	v_and_b32_e32 v0, -8, v0
	v_lshlrev_b32_e32 v2, 11, v2
	s_or_b32 s12, s12, s69
	v_add3_u32 v0, s12, v0, v2
	v_lshlrev_b64 v[10:11], 1, v[0:1]
	v_lshl_add_u64 v[6:7], s[44:45], 0, v[10:11]
	v_add_u32_e32 v220, 0x0, v0
	v_lshlrev_b32_e32 v220, 1, v220
	global_load_dwordx4 v[16:19], v220, s[44:45]
	v_add_u32_e32 v220, 0x0, v0
	v_lshlrev_b32_e32 v220, 1, v220
	global_load_dwordx4 v[20:23], v220, s[44:45] offset:256
	v_add_u32_e32 v220, 0x8000, v0
	v_lshlrev_b32_e32 v220, 1, v220
	global_load_dwordx4 v[24:27], v220, s[44:45]
	v_add_u32_e32 v220, 0x8000, v0
	v_lshlrev_b32_e32 v220, 1, v220
	global_load_dwordx4 v[28:31], v220, s[44:45] offset:256
	v_add_u32_e32 v220, 0x10000, v0
	v_lshlrev_b32_e32 v220, 1, v220
	global_load_dwordx4 v[172:175], v220, s[44:45]
	v_add_u32_e32 v220, 0x10000, v0
	v_lshlrev_b32_e32 v220, 1, v220
	global_load_dwordx4 v[176:179], v220, s[44:45] offset:256
	v_add_u32_e32 v220, 0x18000, v0
	v_lshlrev_b32_e32 v220, 1, v220
	global_load_dwordx4 v[186:189], v220, s[44:45]
	v_add_u32_e32 v220, 0x18000, v0
	v_lshlrev_b32_e32 v220, 1, v220
	global_load_dwordx4 v[190:193], v220, s[44:45] offset:256
	v_add_u32_e32 v220, 0x40000, v0
	v_lshlrev_b32_e32 v220, 1, v220
	global_load_dwordx4 v[194:197], v220, s[44:45]
	v_add_u32_e32 v220, 0x40000, v0
	v_lshlrev_b32_e32 v220, 1, v220
	global_load_dwordx4 v[198:201], v220, s[44:45] offset:256
	v_add_u32_e32 v220, 0x48000, v0
	v_lshlrev_b32_e32 v220, 1, v220
	global_load_dwordx4 v[202:205], v220, s[44:45]
	v_add_u32_e32 v220, 0x48000, v0
	v_lshlrev_b32_e32 v220, 1, v220
	global_load_dwordx4 v[206:209], v220, s[44:45] offset:256
	v_add_u32_e32 v220, 0x50000, v0
	v_lshlrev_b32_e32 v220, 1, v220
	global_load_dwordx4 v[212:215], v220, s[44:45]
	v_add_u32_e32 v220, 0x50000, v0
	v_lshlrev_b32_e32 v220, 1, v220
	global_load_dwordx4 v[216:219], v220, s[44:45] offset:256
	v_lshl_add_u64 v[10:11], s[46:47], 0, v[10:11]
	s_and_b64 vcc, exec, s[38:39]
	s_mov_b64 s[38:39], -1
	s_waitcnt vmcnt(13)
	v_lshlrev_b32_e32 v8, 16, v16
	v_and_b32_e32 v9, 0xffff0000, v16
	v_lshlrev_b32_e32 v2, 16, v17
	v_and_b32_e32 v3, 0xffff0000, v17
	v_lshlrev_b32_e32 v12, 16, v18
	v_and_b32_e32 v13, 0xffff0000, v18
	v_lshlrev_b32_e32 v4, 16, v19
	v_and_b32_e32 v5, 0xffff0000, v19
	v_pk_fma_f32 v[14:15], v[2:3], s[16:17], v[160:161] op_sel_hi:[1,0,1]
	v_pk_fma_f32 v[2:3], v[8:9], s[16:17], v[158:159] op_sel_hi:[1,0,1]
	v_pk_fma_f32 v[8:9], v[4:5], s[16:17], v[156:157] op_sel_hi:[1,0,1]
	v_pk_fma_f32 v[4:5], v[12:13], s[16:17], v[154:155] op_sel_hi:[1,0,1]
	v_cvt_pk_bf16_f32 v2, v2, v3
	v_cvt_pk_bf16_f32 v3, v14, v15
	v_mov_b32_e32 v13, v1
	v_cvt_pk_bf16_f32 v4, v4, v5
	v_cvt_pk_bf16_f32 v5, v8, v9
	v_add_u32_e32 v220, 0x58000, v0
	v_lshlrev_b32_e32 v220, 1, v220
	global_load_dwordx4 v[16:19], v220, s[44:45]
	v_add_u32_e32 v12, 0x8000, v0
	global_store_dwordx4 v[10:11], v[2:5], off
	v_lshlrev_b64 v[12:13], 1, v[12:13]
	v_lshl_add_u64 v[14:15], s[44:45], 0, v[12:13]
	v_lshl_add_u64 v[12:13], s[46:47], 0, v[12:13]
	s_waitcnt vmcnt(14)
	v_lshlrev_b32_e32 v2, 16, v20
	v_and_b32_e32 v3, 0xffff0000, v20
	v_lshlrev_b32_e32 v4, 16, v21
	v_and_b32_e32 v5, 0xffff0000, v21
	v_lshlrev_b32_e32 v6, 16, v22
	v_and_b32_e32 v7, 0xffff0000, v22
	v_lshlrev_b32_e32 v8, 16, v23
	v_and_b32_e32 v9, 0xffff0000, v23
	v_pk_fma_f32 v[4:5], v[4:5], s[16:17], v[152:153] op_sel_hi:[1,0,1]
	v_pk_fma_f32 v[2:3], v[2:3], s[16:17], v[150:151] op_sel_hi:[1,0,1]
	v_pk_fma_f32 v[8:9], v[8:9], s[16:17], v[148:149] op_sel_hi:[1,0,1]
	v_pk_fma_f32 v[6:7], v[6:7], s[16:17], v[146:147] op_sel_hi:[1,0,1]
	v_cvt_pk_bf16_f32 v2, v2, v3
	v_cvt_pk_bf16_f32 v3, v4, v5
	s_nop 0
	v_cvt_pk_bf16_f32 v4, v6, v7
	v_cvt_pk_bf16_f32 v5, v8, v9
	global_store_dwordx4 v[10:11], v[2:5], off offset:256
	v_add_u32_e32 v220, 0x58000, v0
	v_lshlrev_b32_e32 v220, 1, v220
	global_load_dwordx4 v[20:23], v220, s[44:45] offset:256
	s_waitcnt vmcnt(15)
	v_lshlrev_b32_e32 v6, 16, v24
	v_and_b32_e32 v7, 0xffff0000, v24
	v_lshlrev_b32_e32 v2, 16, v25
	v_and_b32_e32 v3, 0xffff0000, v25
	v_lshlrev_b32_e32 v8, 16, v26
	v_and_b32_e32 v9, 0xffff0000, v26
	v_lshlrev_b32_e32 v4, 16, v27
	v_and_b32_e32 v5, 0xffff0000, v27
	v_pk_fma_f32 v[10:11], v[2:3], s[16:17], v[144:145] op_sel_hi:[1,0,1]
	v_pk_fma_f32 v[2:3], v[6:7], s[16:17], v[142:143] op_sel_hi:[1,0,1]
	v_pk_fma_f32 v[6:7], v[4:5], s[16:17], v[140:141] op_sel_hi:[1,0,1]
	v_pk_fma_f32 v[4:5], v[8:9], s[16:17], v[138:139] op_sel_hi:[1,0,1]
	v_cvt_pk_bf16_f32 v2, v2, v3
	v_cvt_pk_bf16_f32 v3, v10, v11
	v_mov_b32_e32 v11, v1
	v_cvt_pk_bf16_f32 v4, v4, v5
	v_cvt_pk_bf16_f32 v5, v6, v7
	v_add_u32_e32 v10, 0x10000, v0
	global_store_dwordx4 v[12:13], v[2:5], off
	v_lshlrev_b64 v[10:11], 1, v[10:11]
	v_lshl_add_u64 v[14:15], s[44:45], 0, v[10:11]
	v_lshl_add_u64 v[10:11], s[46:47], 0, v[10:11]
	s_waitcnt vmcnt(15)
	v_lshlrev_b32_e32 v2, 16, v28
	v_and_b32_e32 v3, 0xffff0000, v28
	v_lshlrev_b32_e32 v4, 16, v29
	v_and_b32_e32 v5, 0xffff0000, v29
	v_lshlrev_b32_e32 v6, 16, v30
	v_and_b32_e32 v7, 0xffff0000, v30
	v_lshlrev_b32_e32 v8, 16, v31
	v_and_b32_e32 v9, 0xffff0000, v31
	v_pk_fma_f32 v[4:5], v[4:5], s[16:17], v[136:137] op_sel_hi:[1,0,1]
	v_pk_fma_f32 v[2:3], v[2:3], s[16:17], v[134:135] op_sel_hi:[1,0,1]
	v_pk_fma_f32 v[8:9], v[8:9], s[16:17], v[132:133] op_sel_hi:[1,0,1]
	v_pk_fma_f32 v[6:7], v[6:7], s[16:17], v[130:131] op_sel_hi:[1,0,1]
	v_cvt_pk_bf16_f32 v2, v2, v3
	v_cvt_pk_bf16_f32 v3, v4, v5
	s_nop 0
	v_cvt_pk_bf16_f32 v4, v6, v7
	v_cvt_pk_bf16_f32 v5, v8, v9
	global_store_dwordx4 v[12:13], v[2:5], off offset:256
	s_waitcnt vmcnt(15)
	v_lshlrev_b32_e32 v6, 16, v172
	v_and_b32_e32 v7, 0xffff0000, v172
	v_lshlrev_b32_e32 v2, 16, v173
	v_and_b32_e32 v3, 0xffff0000, v173
	v_lshlrev_b32_e32 v8, 16, v174
	v_and_b32_e32 v9, 0xffff0000, v174
	v_lshlrev_b32_e32 v4, 16, v175
	v_and_b32_e32 v5, 0xffff0000, v175
	v_pk_fma_f32 v[12:13], v[2:3], s[16:17], v[128:129] op_sel_hi:[1,0,1]
	v_pk_fma_f32 v[2:3], v[6:7], s[16:17], v[126:127] op_sel_hi:[1,0,1]
	v_pk_fma_f32 v[6:7], v[4:5], s[16:17], v[124:125] op_sel_hi:[1,0,1]
	v_pk_fma_f32 v[4:5], v[8:9], s[16:17], v[122:123] op_sel_hi:[1,0,1]
	v_cvt_pk_bf16_f32 v2, v2, v3
	v_cvt_pk_bf16_f32 v3, v12, v13
	v_mov_b32_e32 v13, v1
	v_cvt_pk_bf16_f32 v4, v4, v5
	v_cvt_pk_bf16_f32 v5, v6, v7
	v_add_u32_e32 v12, 0x18000, v0
	global_store_dwordx4 v[10:11], v[2:5], off
	v_lshlrev_b64 v[12:13], 1, v[12:13]
	v_lshl_add_u64 v[14:15], s[44:45], 0, v[12:13]
	v_lshl_add_u64 v[12:13], s[46:47], 0, v[12:13]
	s_waitcnt vmcnt(15)
	v_lshlrev_b32_e32 v2, 16, v176
	v_and_b32_e32 v3, 0xffff0000, v176
	v_lshlrev_b32_e32 v4, 16, v177
	v_and_b32_e32 v5, 0xffff0000, v177
	v_lshlrev_b32_e32 v6, 16, v178
	v_and_b32_e32 v7, 0xffff0000, v178
	v_lshlrev_b32_e32 v8, 16, v179
	v_and_b32_e32 v9, 0xffff0000, v179
	v_pk_fma_f32 v[4:5], v[4:5], s[16:17], v[120:121] op_sel_hi:[1,0,1]
	v_pk_fma_f32 v[2:3], v[2:3], s[16:17], v[118:119] op_sel_hi:[1,0,1]
	v_pk_fma_f32 v[8:9], v[8:9], s[16:17], v[116:117] op_sel_hi:[1,0,1]
	v_pk_fma_f32 v[6:7], v[6:7], s[16:17], v[114:115] op_sel_hi:[1,0,1]
	v_cvt_pk_bf16_f32 v2, v2, v3
	v_cvt_pk_bf16_f32 v3, v4, v5
	s_nop 0
	v_cvt_pk_bf16_f32 v4, v6, v7
	v_cvt_pk_bf16_f32 v5, v8, v9
	global_store_dwordx4 v[10:11], v[2:5], off offset:256
	s_waitcnt vmcnt(15)
	v_lshlrev_b32_e32 v6, 16, v186
	v_and_b32_e32 v7, 0xffff0000, v186
	v_lshlrev_b32_e32 v2, 16, v187
	v_and_b32_e32 v3, 0xffff0000, v187
	v_lshlrev_b32_e32 v8, 16, v188
	v_and_b32_e32 v9, 0xffff0000, v188
	v_lshlrev_b32_e32 v4, 16, v189
	v_and_b32_e32 v5, 0xffff0000, v189
	v_pk_fma_f32 v[10:11], v[2:3], s[16:17], v[112:113] op_sel_hi:[1,0,1]
	v_pk_fma_f32 v[2:3], v[6:7], s[16:17], v[110:111] op_sel_hi:[1,0,1]
	v_pk_fma_f32 v[6:7], v[4:5], s[16:17], v[108:109] op_sel_hi:[1,0,1]
	v_pk_fma_f32 v[4:5], v[8:9], s[16:17], v[106:107] op_sel_hi:[1,0,1]
	v_cvt_pk_bf16_f32 v2, v2, v3
	v_cvt_pk_bf16_f32 v3, v10, v11
	v_mov_b32_e32 v11, v1
	v_cvt_pk_bf16_f32 v4, v4, v5
	v_cvt_pk_bf16_f32 v5, v6, v7
	v_add_u32_e32 v10, 0x40000, v0
	global_store_dwordx4 v[12:13], v[2:5], off
	v_lshlrev_b64 v[10:11], 1, v[10:11]
	v_lshl_add_u64 v[14:15], s[44:45], 0, v[10:11]
	v_lshl_add_u64 v[10:11], s[46:47], 0, v[10:11]
	s_waitcnt vmcnt(15)
	v_lshlrev_b32_e32 v2, 16, v190
	v_and_b32_e32 v3, 0xffff0000, v190
	v_lshlrev_b32_e32 v4, 16, v191
	v_and_b32_e32 v5, 0xffff0000, v191
	v_lshlrev_b32_e32 v6, 16, v192
	v_and_b32_e32 v7, 0xffff0000, v192
	v_lshlrev_b32_e32 v8, 16, v193
	v_and_b32_e32 v9, 0xffff0000, v193
	v_pk_fma_f32 v[4:5], v[4:5], s[16:17], v[104:105] op_sel_hi:[1,0,1]
	v_pk_fma_f32 v[2:3], v[2:3], s[16:17], v[102:103] op_sel_hi:[1,0,1]
	v_pk_fma_f32 v[8:9], v[8:9], s[16:17], v[100:101] op_sel_hi:[1,0,1]
	v_pk_fma_f32 v[6:7], v[6:7], s[16:17], v[98:99] op_sel_hi:[1,0,1]
	v_cvt_pk_bf16_f32 v2, v2, v3
	v_cvt_pk_bf16_f32 v3, v4, v5
	s_nop 0
	v_cvt_pk_bf16_f32 v4, v6, v7
	v_cvt_pk_bf16_f32 v5, v8, v9
	global_store_dwordx4 v[12:13], v[2:5], off offset:256
	s_waitcnt vmcnt(15)
	v_lshlrev_b32_e32 v6, 16, v194
	v_and_b32_e32 v7, 0xffff0000, v194
	v_lshlrev_b32_e32 v2, 16, v195
	v_and_b32_e32 v3, 0xffff0000, v195
	v_lshlrev_b32_e32 v8, 16, v196
	v_and_b32_e32 v9, 0xffff0000, v196
	v_lshlrev_b32_e32 v4, 16, v197
	v_and_b32_e32 v5, 0xffff0000, v197
	v_pk_fma_f32 v[12:13], v[2:3], s[16:17], v[96:97] op_sel_hi:[1,0,1]
	v_pk_fma_f32 v[2:3], v[6:7], s[16:17], v[94:95] op_sel_hi:[1,0,1]
	v_pk_fma_f32 v[6:7], v[4:5], s[16:17], v[92:93] op_sel_hi:[1,0,1]
	v_pk_fma_f32 v[4:5], v[8:9], s[16:17], v[90:91] op_sel_hi:[1,0,1]
	v_cvt_pk_bf16_f32 v2, v2, v3
	v_cvt_pk_bf16_f32 v3, v12, v13
	v_mov_b32_e32 v13, v1
	v_cvt_pk_bf16_f32 v4, v4, v5
	v_cvt_pk_bf16_f32 v5, v6, v7
	v_add_u32_e32 v12, 0x48000, v0
	global_store_dwordx4 v[10:11], v[2:5], off
	v_lshlrev_b64 v[12:13], 1, v[12:13]
	v_lshl_add_u64 v[14:15], s[44:45], 0, v[12:13]
	v_lshl_add_u64 v[12:13], s[46:47], 0, v[12:13]
	s_waitcnt vmcnt(15)
	v_lshlrev_b32_e32 v2, 16, v198
	v_and_b32_e32 v3, 0xffff0000, v198
	v_lshlrev_b32_e32 v4, 16, v199
	v_and_b32_e32 v5, 0xffff0000, v199
	v_lshlrev_b32_e32 v6, 16, v200
	v_and_b32_e32 v7, 0xffff0000, v200
	v_lshlrev_b32_e32 v8, 16, v201
	v_and_b32_e32 v9, 0xffff0000, v201
	v_pk_fma_f32 v[4:5], v[4:5], s[16:17], v[88:89] op_sel_hi:[1,0,1]
	v_pk_fma_f32 v[2:3], v[2:3], s[16:17], v[86:87] op_sel_hi:[1,0,1]
	v_pk_fma_f32 v[8:9], v[8:9], s[16:17], v[84:85] op_sel_hi:[1,0,1]
	v_pk_fma_f32 v[6:7], v[6:7], s[16:17], v[82:83] op_sel_hi:[1,0,1]
	v_cvt_pk_bf16_f32 v2, v2, v3
	v_cvt_pk_bf16_f32 v3, v4, v5
	s_nop 0
	v_cvt_pk_bf16_f32 v4, v6, v7
	v_cvt_pk_bf16_f32 v5, v8, v9
	global_store_dwordx4 v[10:11], v[2:5], off offset:256
	s_waitcnt vmcnt(15)
	v_lshlrev_b32_e32 v6, 16, v202
	v_and_b32_e32 v7, 0xffff0000, v202
	v_lshlrev_b32_e32 v2, 16, v203
	v_and_b32_e32 v3, 0xffff0000, v203
	v_lshlrev_b32_e32 v8, 16, v204
	v_and_b32_e32 v9, 0xffff0000, v204
	v_lshlrev_b32_e32 v4, 16, v205
	v_and_b32_e32 v5, 0xffff0000, v205
	v_pk_fma_f32 v[10:11], v[2:3], s[16:17], v[80:81] op_sel_hi:[1,0,1]
	v_pk_fma_f32 v[2:3], v[6:7], s[16:17], v[78:79] op_sel_hi:[1,0,1]
	v_pk_fma_f32 v[6:7], v[4:5], s[16:17], v[76:77] op_sel_hi:[1,0,1]
	v_pk_fma_f32 v[4:5], v[8:9], s[16:17], v[74:75] op_sel_hi:[1,0,1]
	v_cvt_pk_bf16_f32 v2, v2, v3
	v_cvt_pk_bf16_f32 v3, v10, v11
	v_mov_b32_e32 v11, v1
	v_cvt_pk_bf16_f32 v4, v4, v5
	v_cvt_pk_bf16_f32 v5, v6, v7
	v_add_u32_e32 v10, 0x50000, v0
	global_store_dwordx4 v[12:13], v[2:5], off
	v_lshlrev_b64 v[10:11], 1, v[10:11]
	v_lshl_add_u64 v[14:15], s[44:45], 0, v[10:11]
	v_lshl_add_u64 v[10:11], s[46:47], 0, v[10:11]
	v_add_u32_e32 v0, 0x58000, v0
	s_waitcnt vmcnt(15)
	v_lshlrev_b32_e32 v2, 16, v206
	v_and_b32_e32 v3, 0xffff0000, v206
	v_lshlrev_b32_e32 v4, 16, v207
	v_and_b32_e32 v5, 0xffff0000, v207
	v_lshlrev_b32_e32 v6, 16, v208
	v_and_b32_e32 v7, 0xffff0000, v208
	v_lshlrev_b32_e32 v8, 16, v209
	v_and_b32_e32 v9, 0xffff0000, v209
	v_pk_fma_f32 v[4:5], v[4:5], s[16:17], v[72:73] op_sel_hi:[1,0,1]
	v_pk_fma_f32 v[2:3], v[2:3], s[16:17], v[70:71] op_sel_hi:[1,0,1]
	v_pk_fma_f32 v[8:9], v[8:9], s[16:17], v[68:69] op_sel_hi:[1,0,1]
	v_pk_fma_f32 v[6:7], v[6:7], s[16:17], v[66:67] op_sel_hi:[1,0,1]
	v_cvt_pk_bf16_f32 v2, v2, v3
	v_cvt_pk_bf16_f32 v3, v4, v5
	s_nop 0
	v_cvt_pk_bf16_f32 v4, v6, v7
	v_cvt_pk_bf16_f32 v5, v8, v9
	global_store_dwordx4 v[12:13], v[2:5], off offset:256
	s_waitcnt vmcnt(15)
	v_lshlrev_b32_e32 v6, 16, v212
	v_and_b32_e32 v7, 0xffff0000, v212
	v_lshlrev_b32_e32 v2, 16, v213
	v_and_b32_e32 v3, 0xffff0000, v213
	v_lshlrev_b32_e32 v8, 16, v214
	v_and_b32_e32 v9, 0xffff0000, v214
	v_lshlrev_b32_e32 v4, 16, v215
	v_and_b32_e32 v5, 0xffff0000, v215
	v_pk_fma_f32 v[12:13], v[2:3], s[16:17], v[64:65] op_sel_hi:[1,0,1]
	v_pk_fma_f32 v[2:3], v[6:7], s[16:17], v[62:63] op_sel_hi:[1,0,1]
	v_pk_fma_f32 v[6:7], v[4:5], s[16:17], v[60:61] op_sel_hi:[1,0,1]
	v_pk_fma_f32 v[4:5], v[8:9], s[16:17], v[58:59] op_sel_hi:[1,0,1]
	v_cvt_pk_bf16_f32 v2, v2, v3
	v_cvt_pk_bf16_f32 v3, v12, v13
	v_lshlrev_b64 v[12:13], 1, v[0:1]
	v_cvt_pk_bf16_f32 v4, v4, v5
	v_cvt_pk_bf16_f32 v5, v6, v7
	v_lshl_add_u64 v[14:15], s[44:45], 0, v[12:13]
	global_store_dwordx4 v[10:11], v[2:5], off
	s_waitcnt vmcnt(15)
	s_nop 0
	v_lshlrev_b32_e32 v2, 16, v216
	v_and_b32_e32 v3, 0xffff0000, v216
	v_lshlrev_b32_e32 v4, 16, v217
	v_and_b32_e32 v5, 0xffff0000, v217
	v_lshlrev_b32_e32 v6, 16, v218
	v_and_b32_e32 v7, 0xffff0000, v218
	v_lshlrev_b32_e32 v8, 16, v219
	v_and_b32_e32 v9, 0xffff0000, v219
	v_pk_fma_f32 v[4:5], v[4:5], s[16:17], v[56:57] op_sel_hi:[1,0,1]
	v_pk_fma_f32 v[2:3], v[2:3], s[16:17], v[54:55] op_sel_hi:[1,0,1]
	v_pk_fma_f32 v[8:9], v[8:9], s[16:17], v[52:53] op_sel_hi:[1,0,1]
	v_pk_fma_f32 v[6:7], v[6:7], s[16:17], v[50:51] op_sel_hi:[1,0,1]
	v_cvt_pk_bf16_f32 v2, v2, v3
	v_cvt_pk_bf16_f32 v3, v4, v5
	s_nop 0
	v_cvt_pk_bf16_f32 v4, v6, v7
	v_cvt_pk_bf16_f32 v5, v8, v9
	global_store_dwordx4 v[10:11], v[2:5], off offset:256
	s_waitcnt vmcnt(15)
	v_lshlrev_b32_e32 v6, 16, v16
	v_and_b32_e32 v7, 0xffff0000, v16
	v_lshlrev_b32_e32 v2, 16, v17
	v_and_b32_e32 v3, 0xffff0000, v17
	v_lshlrev_b32_e32 v8, 16, v18
	v_and_b32_e32 v9, 0xffff0000, v18
	v_lshlrev_b32_e32 v4, 16, v19
	v_and_b32_e32 v5, 0xffff0000, v19
	v_pk_fma_f32 v[10:11], v[2:3], s[16:17], v[48:49] op_sel_hi:[1,0,1]
	v_pk_fma_f32 v[2:3], v[6:7], s[16:17], v[46:47] op_sel_hi:[1,0,1]
	v_pk_fma_f32 v[6:7], v[4:5], s[16:17], v[44:45] op_sel_hi:[1,0,1]
	v_pk_fma_f32 v[4:5], v[8:9], s[16:17], v[42:43] op_sel_hi:[1,0,1]
	v_cvt_pk_bf16_f32 v2, v2, v3
	v_cvt_pk_bf16_f32 v3, v10, v11
	v_lshl_add_u64 v[10:11], s[46:47], 0, v[12:13]
	v_cvt_pk_bf16_f32 v4, v4, v5
	v_cvt_pk_bf16_f32 v5, v6, v7
	s_nop 0
	global_store_dwordx4 v[10:11], v[2:5], off
	s_waitcnt vmcnt(13)
	s_nop 0
	v_lshlrev_b32_e32 v2, 16, v20
	v_and_b32_e32 v3, 0xffff0000, v20
	v_lshlrev_b32_e32 v4, 16, v21
	v_and_b32_e32 v5, 0xffff0000, v21
	v_lshlrev_b32_e32 v6, 16, v22
	v_and_b32_e32 v7, 0xffff0000, v22
	v_lshlrev_b32_e32 v8, 16, v23
	v_and_b32_e32 v9, 0xffff0000, v23
	v_pk_fma_f32 v[4:5], v[4:5], s[16:17], v[40:41] op_sel_hi:[1,0,1]
	v_pk_fma_f32 v[2:3], v[2:3], s[16:17], v[38:39] op_sel_hi:[1,0,1]
	v_pk_fma_f32 v[8:9], v[8:9], s[16:17], v[36:37] op_sel_hi:[1,0,1]
	v_pk_fma_f32 v[6:7], v[6:7], s[16:17], v[34:35] op_sel_hi:[1,0,1]
	v_cvt_pk_bf16_f32 v2, v2, v3
	v_cvt_pk_bf16_f32 v3, v4, v5
	s_nop 0
	v_cvt_pk_bf16_f32 v4, v6, v7
	v_cvt_pk_bf16_f32 v5, v8, v9
	global_store_dwordx4 v[10:11], v[2:5], off offset:256
	s_cbranch_vccnz .LBB0_804
	s_andn2_b64 vcc, exec, s[42:43]
	s_cbranch_vccnz .LBB0_803
	s_barrier
	s_branch .LBB0_803

	.amdhsa_kernel _Z3fwd4Args
		.amdhsa_group_segment_fixed_size 0
		.amdhsa_private_segment_fixed_size 0
		.amdhsa_kernarg_size 504
		.amdhsa_user_sgpr_count 2
		.amdhsa_user_sgpr_dispatch_ptr 0
		.amdhsa_user_sgpr_queue_ptr 0
		.amdhsa_user_sgpr_kernarg_segment_ptr 1
		.amdhsa_user_sgpr_dispatch_id 0
		.amdhsa_user_sgpr_kernarg_preload_length 0
		.amdhsa_user_sgpr_kernarg_preload_offset 0
		.amdhsa_user_sgpr_private_segment_size 0
		.amdhsa_uses_dynamic_stack 0
		.amdhsa_enable_private_segment 0
		.amdhsa_system_sgpr_workgroup_id_x 1
		.amdhsa_system_sgpr_workgroup_id_y 0
		.amdhsa_system_sgpr_workgroup_id_z 0
		.amdhsa_system_sgpr_workgroup_info 0
		.amdhsa_system_vgpr_workitem_id 0
		.amdhsa_next_free_vgpr 256
		.amdhsa_next_free_sgpr 102
		.amdhsa_accum_offset 256
		.amdhsa_reserve_vcc 1
		.amdhsa_float_round_mode_32 0
		.amdhsa_float_round_mode_16_64 0
		.amdhsa_float_denorm_mode_32 3
		.amdhsa_float_denorm_mode_16_64 3
		.amdhsa_dx10_clamp 1
		.amdhsa_ieee_mode 1
		.amdhsa_fp16_overflow 0
		.amdhsa_tg_split 0
		.amdhsa_exception_fp_ieee_invalid_op 0
		.amdhsa_exception_fp_denorm_src 0
		.amdhsa_exception_fp_ieee_div_zero 0
		.amdhsa_exception_fp_ieee_overflow 0
		.amdhsa_exception_fp_ieee_underflow 0
		.amdhsa_exception_fp_ieee_inexact 0
		.amdhsa_exception_int_div_zero 0
	.end_amdhsa_kernel

amdhsa.kernels:
  - .agpr_count:     0
    .args:
      - .offset:         0
        .size:           248
        .value_kind:     by_value
      - .offset:         248
        .size:           4
        .value_kind:     hidden_block_count_x
      - .offset:         252
        .size:           4
        .value_kind:     hidden_block_count_y
      - .offset:         256
        .size:           4
        .value_kind:     hidden_block_count_z
      - .offset:         260
        .size:           2
        .value_kind:     hidden_group_size_x
      - .offset:         262
        .size:           2
        .value_kind:     hidden_group_size_y
      - .offset:         264
        .size:           2
        .value_kind:     hidden_group_size_z
      - .offset:         266
        .size:           2
        .value_kind:     hidden_remainder_x
      - .offset:         268
        .size:           2
        .value_kind:     hidden_remainder_y
      - .offset:         270
        .size:           2
        .value_kind:     hidden_remainder_z
      - .offset:         288
        .size:           8
        .value_kind:     hidden_global_offset_x
      - .offset:         296
        .size:           8
        .value_kind:     hidden_global_offset_y
      - .offset:         304
        .size:           8
        .value_kind:     hidden_global_offset_z
      - .offset:         312
        .size:           2
        .value_kind:     hidden_grid_dims
      - .offset:         368
        .size:           4
        .value_kind:     hidden_dynamic_lds_size
    .group_segment_fixed_size: 0
    .kernarg_segment_align: 8
    .kernarg_segment_size: 504
    .language:       OpenCL C
    .language_version:
      - 2
      - 0
    .max_flat_workgroup_size: 512
    .name:           _Z3fwd4Args
    .private_segment_fixed_size: 0
    .sgpr_count:     108
    .sgpr_spill_count: 219
    .symbol:         _Z3fwd4Args.kd
    .uniform_work_group_size: 1
    .uses_dynamic_stack: false
    .vgpr_count:     256
    .vgpr_spill_count: 0
    .wavefront_size: 64
